# weight-transpose staging loops of the in-phase prep (non-scan half): the 16 row loads of an iteration issued together, LDS writes behind counted vmcnt waits (on top of gMLP + scan rewrites)
# speedup vs baseline: 1.0305x; 1.0043x over previous
; __device__ __forceinline__ unsigned cvt_pk_bf16(float lo, float hi) { unsigned r; asm volatile("v_cvt_pk_bf16_f32 %0, %1, %2" : "=v"(r) : "v"(lo), "v"(hi)); return r; }
; #define LAS __attribute__((address_space(3)))
;     const int nblk = ncols / 32, kb = item / nblk, nb = item % nblk, k0 = 64 * kb, n0 = 32 * nb;
; #pragma unroll 8
;     for (int i = 0; i < 32; ++i) { const int kk = 2 * i + (lane >> 5); scr[kk * 33 + (lane & 31)] = W[(size_t)(k0 + kk) * ldw + n0 + (lane & 31)]; }
;     asm volatile("s_waitcnt lgkmcnt(0)" ::: "memory");
;     const int c = lane & 7;
; #pragma unroll
;     for (int j = 0; j < 4; ++j) { const int n = (lane >> 3) + 8 * j; const LAS float* s = scr + (8 * c) * 33 + n;
;         v4u o; o.x = cvt_pk_bf16(s[0 * 33], s[1 * 33]); o.y = cvt_pk_bf16(s[2 * 33], s[3 * 33]); o.z = cvt_pk_bf16(s[4 * 33], s[5 * 33]); o.w = cvt_pk_bf16(s[6 * 33], s[7 * 33]);
;         *(v4u*)(WT + (size_t)(row_off + n0 + n) * ldt + ((koff + k0 + 8 * c) ^ kx)) = o; }
;     asm volatile("s_waitcnt lgkmcnt(0)" ::: "memory");
.LBB0_1189:
	s_lshl_b32 s36, s22, 1
	s_lshl_b32 s37, s21, 1
	v_add_u32_e32 v42, s36, v24
	v_add_u32_e32 v44, s37, v19
	v_mad_i64_i32 v[42:43], s[38:39], v42, s80, v[22:23]
	v_mad_i64_i32 v[44:45], s[38:39], v44, s80, v[22:23]
	global_load_dword v100, v[42:43], off
	global_load_dword v101, v[44:45], off
	v_add_u32_e32 v47, s36, v2
	v_add_u32_e32 v46, s37, v1
	v_mad_u64_u32 v[116:117], s[38:39], v47, s26, v[4:5]
	v_mad_u64_u32 v[118:119], s[38:39], v46, s26, v[4:5]
	v_add_u32_e32 v47, s36, v8
	v_add_u32_e32 v46, s37, v3
	s_add_i32 s22, s22, 16
	s_add_i32 s21, s21, 16
	s_add_i32 s30, s30, -16
	s_cmp_lg_u32 s30, 0
	v_add_u32_e32 v42, s36, v26
	v_add_u32_e32 v44, s37, v21
	v_mad_i64_i32 v[42:43], s[38:39], v42, s80, v[22:23]
	v_mad_i64_i32 v[44:45], s[38:39], v44, s80, v[22:23]
	global_load_dword v102, v[42:43], off
	global_load_dword v103, v[44:45], off
	v_mad_u64_u32 v[120:121], s[38:39], v47, s26, v[4:5]
	v_mad_u64_u32 v[122:123], s[38:39], v46, s26, v[4:5]
	v_add_u32_e32 v47, s36, v10
	v_add_u32_e32 v46, s37, v5
	v_add_u32_e32 v42, s36, v28
	v_add_u32_e32 v44, s37, v25
	v_mad_i64_i32 v[42:43], s[38:39], v42, s80, v[22:23]
	v_mad_i64_i32 v[44:45], s[38:39], v44, s80, v[22:23]
	global_load_dword v104, v[42:43], off
	global_load_dword v105, v[44:45], off
	v_mad_u64_u32 v[124:125], s[38:39], v47, s26, v[4:5]
	v_mad_u64_u32 v[126:127], s[38:39], v46, s26, v[4:5]
	v_add_u32_e32 v47, s36, v12
	v_add_u32_e32 v46, s37, v9
	v_add_u32_e32 v42, s36, v30
	v_add_u32_e32 v44, s37, v27
	v_mad_i64_i32 v[42:43], s[38:39], v42, s80, v[22:23]
	v_mad_i64_i32 v[44:45], s[38:39], v44, s80, v[22:23]
	global_load_dword v106, v[42:43], off
	global_load_dword v107, v[44:45], off
	v_mad_u64_u32 v[128:129], s[38:39], v47, s26, v[4:5]
	v_mad_u64_u32 v[130:131], s[38:39], v46, s26, v[4:5]
	v_add_u32_e32 v47, s36, v14
	v_add_u32_e32 v46, s37, v11
	v_add_u32_e32 v42, s36, v32
	v_add_u32_e32 v44, s37, v29
	v_mad_i64_i32 v[42:43], s[38:39], v42, s80, v[22:23]
	v_mad_i64_i32 v[44:45], s[38:39], v44, s80, v[22:23]
	global_load_dword v108, v[42:43], off
	global_load_dword v109, v[44:45], off
	v_mad_u64_u32 v[132:133], s[38:39], v47, s26, v[4:5]
	v_mad_u64_u32 v[134:135], s[38:39], v46, s26, v[4:5]
	v_add_u32_e32 v47, s36, v16
	v_add_u32_e32 v46, s37, v13
	v_add_u32_e32 v42, s36, v34
	v_add_u32_e32 v44, s37, v31
	v_mad_i64_i32 v[42:43], s[38:39], v42, s80, v[22:23]
	v_mad_i64_i32 v[44:45], s[38:39], v44, s80, v[22:23]
	global_load_dword v110, v[42:43], off
	global_load_dword v111, v[44:45], off
	v_mad_u64_u32 v[136:137], s[38:39], v47, s26, v[4:5]
	v_mad_u64_u32 v[138:139], s[38:39], v46, s26, v[4:5]
	v_add_u32_e32 v47, s36, v18
	v_add_u32_e32 v46, s37, v15
	v_add_u32_e32 v42, s36, v36
	v_add_u32_e32 v44, s37, v33
	v_mad_i64_i32 v[42:43], s[38:39], v42, s80, v[22:23]
	v_mad_i64_i32 v[44:45], s[38:39], v44, s80, v[22:23]
	global_load_dword v112, v[42:43], off
	global_load_dword v113, v[44:45], off
	v_mad_u64_u32 v[140:141], s[38:39], v47, s26, v[4:5]
	v_mad_u64_u32 v[142:143], s[38:39], v46, s26, v[4:5]
	v_add_u32_e32 v46, s37, v17
	v_add_u32_e32 v47, s36, v20
	v_add_u32_e32 v42, s36, v38
	v_add_u32_e32 v44, s37, v35
	v_mad_i64_i32 v[42:43], s[36:37], v42, s80, v[22:23]
	v_mad_i64_i32 v[44:45], s[36:37], v44, s80, v[22:23]
	global_load_dword v114, v[42:43], off
	global_load_dword v115, v[44:45], off
	v_mad_u64_u32 v[144:145], s[36:37], v47, s26, v[4:5]
	v_mad_u64_u32 v[146:147], s[36:37], v46, s26, v[4:5]
	s_waitcnt vmcnt(14)
	ds_write_b32 v116, v100
	ds_write_b32 v118, v101
	s_waitcnt vmcnt(12)
	ds_write_b32 v120, v102
	ds_write_b32 v122, v103
	s_waitcnt vmcnt(10)
	ds_write_b32 v124, v104
	ds_write_b32 v126, v105
	s_waitcnt vmcnt(8)
	ds_write_b32 v128, v106
	ds_write_b32 v130, v107
	s_waitcnt vmcnt(6)
	ds_write_b32 v132, v108
	ds_write_b32 v134, v109
	s_waitcnt vmcnt(4)
	ds_write_b32 v136, v110
	ds_write_b32 v138, v111
	s_waitcnt vmcnt(2)
	ds_write_b32 v140, v112
	ds_write_b32 v142, v113
	s_waitcnt vmcnt(0)
	ds_write_b32 v144, v114
	ds_write_b32 v146, v115
	s_cbranch_scc1 .LBB0_1189
	v_mov_b32_e32 v19, 0x400
	v_bitop3_b32 v22, s23, v19, v40 bitop3:0x36
	s_waitcnt lgkmcnt(0)
	v_ashrrev_i32_e32 v23, 31, v22
	v_lshl_add_u64 v[26:27], v[22:23], 1, s[2:3]
	ds_read2_b32 v[22:23], v41 offset1:33
	s_waitcnt lgkmcnt(0)
	v_cvt_pk_bf16_f32 v22, v22, v23
	ds_read2_b32 v[24:25], v41 offset0:66 offset1:99
	s_waitcnt lgkmcnt(0)
	v_cvt_pk_bf16_f32 v23, v24, v25
	ds_read2_b32 v[24:25], v41 offset0:132 offset1:165
	s_waitcnt lgkmcnt(0)
	v_cvt_pk_bf16_f32 v24, v24, v25
	ds_read2_b32 v[28:29], v41 offset0:198 offset1:231
	s_waitcnt lgkmcnt(0)
	v_cvt_pk_bf16_f32 v25, v28, v29
	v_add_u32_e32 v28, s20, v39
	v_ashrrev_i32_e32 v29, 31, v28
	v_lshlrev_b64 v[30:31], 12, v[28:29]
	v_lshl_add_u64 v[30:31], v[26:27], 0, v[30:31]
	global_store_dwordx4 v[30:31], v[22:25], off
	ds_read2_b32 v[22:23], v41 offset0:8 offset1:41
	v_readlane_b32 s20, v254, 44
	s_waitcnt lgkmcnt(0)
	v_cvt_pk_bf16_f32 v22, v22, v23
	ds_read2_b32 v[24:25], v41 offset0:74 offset1:107
	s_waitcnt lgkmcnt(0)
	v_cvt_pk_bf16_f32 v23, v24, v25
	ds_read2_b32 v[24:25], v41 offset0:140 offset1:173
	s_waitcnt lgkmcnt(0)
	v_cvt_pk_bf16_f32 v24, v24, v25
	ds_read2_b32 v[30:31], v41 offset0:206 offset1:239
	s_waitcnt lgkmcnt(0)
	v_cvt_pk_bf16_f32 v25, v30, v31
	v_add_u32_e32 v30, 8, v28
	v_ashrrev_i32_e32 v31, 31, v30
	v_lshlrev_b64 v[30:31], 12, v[30:31]
	v_lshl_add_u64 v[30:31], v[26:27], 0, v[30:31]
	global_store_dwordx4 v[30:31], v[22:25], off
	ds_read2_b32 v[22:23], v41 offset0:16 offset1:49
	s_add_i32 s5, s5, s20
	s_waitcnt lgkmcnt(0)
	v_cvt_pk_bf16_f32 v22, v22, v23
	ds_read2_b32 v[24:25], v41 offset0:82 offset1:115
	s_waitcnt lgkmcnt(0)
	v_cvt_pk_bf16_f32 v23, v24, v25
	ds_read2_b32 v[24:25], v41 offset0:148 offset1:181
	s_waitcnt lgkmcnt(0)
	v_cvt_pk_bf16_f32 v24, v24, v25
	ds_read2_b32 v[30:31], v41 offset0:214 offset1:247
	s_waitcnt lgkmcnt(0)
	v_cvt_pk_bf16_f32 v25, v30, v31
	v_add_u32_e32 v30, 16, v28
	v_ashrrev_i32_e32 v31, 31, v30
	v_lshlrev_b64 v[30:31], 12, v[30:31]
	v_lshl_add_u64 v[30:31], v[26:27], 0, v[30:31]
	v_add_u32_e32 v28, 24, v28
	global_store_dwordx4 v[30:31], v[22:25], off
	ds_read2_b32 v[22:23], v41 offset0:24 offset1:57
	v_ashrrev_i32_e32 v29, 31, v28
	s_waitcnt lgkmcnt(0)
	v_cvt_pk_bf16_f32 v22, v22, v23
	ds_read2_b32 v[24:25], v41 offset0:90 offset1:123
	v_lshlrev_b64 v[28:29], 12, v[28:29]
	s_waitcnt lgkmcnt(0)
	v_cvt_pk_bf16_f32 v23, v24, v25
	ds_read2_b32 v[24:25], v41 offset0:156 offset1:189
	v_lshl_add_u64 v[26:27], v[26:27], 0, v[28:29]
	s_waitcnt lgkmcnt(0)
	v_cvt_pk_bf16_f32 v24, v24, v25
	ds_read2_b32 v[30:31], v41 offset0:222 offset1:255
	s_waitcnt lgkmcnt(0)
	v_cvt_pk_bf16_f32 v25, v30, v31
	global_store_dwordx4 v[26:27], v[22:25], off
	s_waitcnt lgkmcnt(0)
	s_cmp_gt_i32 s5, -1
	v_readlane_b32 s21, v254, 45
	s_cbranch_scc0 .LBB0_1188

;     const int nblk = ncols / 32, kb = item / nblk, nb = item % nblk, k0 = 64 * kb, n0 = 32 * nb;
; #pragma unroll 8
;     for (int i = 0; i < 32; ++i) { const int kk = 2 * i + (lane >> 5); scr[kk * 33 + (lane & 31)] = W[(size_t)(k0 + kk) * ldw + n0 + (lane & 31)]; }
;     asm volatile("s_waitcnt lgkmcnt(0)" ::: "memory");
.LBB0_1224:
	s_lshl_b32 s36, s23, 1
	s_lshl_b32 s37, s1, 1
	v_add_u32_e32 v86, s36, v64
	v_add_u32_e32 v84, s37, v55
	v_ashrrev_i32_e32 v87, 31, v86
	v_ashrrev_i32_e32 v85, 31, v84
	v_lshlrev_b64 v[86:87], 12, v[86:87]
	v_lshlrev_b64 v[84:85], 12, v[84:85]
	v_lshl_add_u64 v[86:87], v[62:63], 0, v[86:87]
	v_lshl_add_u64 v[84:85], v[62:63], 0, v[84:85]
	global_load_dword v100, v[86:87], off
	global_load_dword v101, v[84:85], off
	v_add_u32_e32 v88, s37, v1
	v_add_u32_e32 v89, s36, v26
	v_mad_u64_u32 v[116:117], s[38:39], v89, s26, v[28:29]
	v_mad_u64_u32 v[118:119], s[38:39], v88, s26, v[28:29]
	v_add_u32_e32 v88, s37, v3
	v_add_u32_e32 v89, s36, v48
	s_add_i32 s23, s23, 16
	s_add_i32 s1, s1, 16
	s_add_i32 s30, s30, -16
	s_cmp_lg_u32 s30, 0
	v_add_u32_e32 v86, s36, v66
	v_add_u32_e32 v84, s37, v57
	v_ashrrev_i32_e32 v87, 31, v86
	v_ashrrev_i32_e32 v85, 31, v84
	v_lshlrev_b64 v[86:87], 12, v[86:87]
	v_lshlrev_b64 v[84:85], 12, v[84:85]
	v_lshl_add_u64 v[86:87], v[62:63], 0, v[86:87]
	v_lshl_add_u64 v[84:85], v[62:63], 0, v[84:85]
	global_load_dword v102, v[86:87], off
	global_load_dword v103, v[84:85], off
	v_mad_u64_u32 v[120:121], s[38:39], v89, s26, v[28:29]
	v_mad_u64_u32 v[122:123], s[38:39], v88, s26, v[28:29]
	v_add_u32_e32 v88, s37, v27
	v_add_u32_e32 v89, s36, v50
	v_add_u32_e32 v86, s36, v68
	v_add_u32_e32 v84, s37, v59
	v_ashrrev_i32_e32 v87, 31, v86
	v_ashrrev_i32_e32 v85, 31, v84
	v_lshlrev_b64 v[86:87], 12, v[86:87]
	v_lshlrev_b64 v[84:85], 12, v[84:85]
	v_lshl_add_u64 v[86:87], v[62:63], 0, v[86:87]
	v_lshl_add_u64 v[84:85], v[62:63], 0, v[84:85]
	global_load_dword v104, v[86:87], off
	global_load_dword v105, v[84:85], off
	v_mad_u64_u32 v[124:125], s[38:39], v89, s26, v[28:29]
	v_mad_u64_u32 v[126:127], s[38:39], v88, s26, v[28:29]
	v_add_u32_e32 v88, s37, v29
	v_add_u32_e32 v89, s36, v52
	v_add_u32_e32 v86, s36, v70
	v_add_u32_e32 v84, s37, v61
	v_ashrrev_i32_e32 v87, 31, v86
	v_ashrrev_i32_e32 v85, 31, v84
	v_lshlrev_b64 v[86:87], 12, v[86:87]
	v_lshlrev_b64 v[84:85], 12, v[84:85]
	v_lshl_add_u64 v[86:87], v[62:63], 0, v[86:87]
	v_lshl_add_u64 v[84:85], v[62:63], 0, v[84:85]
	global_load_dword v106, v[86:87], off
	global_load_dword v107, v[84:85], off
	v_mad_u64_u32 v[128:129], s[38:39], v89, s26, v[28:29]
	v_mad_u64_u32 v[130:131], s[38:39], v88, s26, v[28:29]
	v_add_u32_e32 v88, s37, v31
	v_add_u32_e32 v89, s36, v54
	v_add_u32_e32 v86, s36, v72
	v_add_u32_e32 v84, s37, v65
	v_ashrrev_i32_e32 v87, 31, v86
	v_ashrrev_i32_e32 v85, 31, v84
	v_lshlrev_b64 v[86:87], 12, v[86:87]
	v_lshlrev_b64 v[84:85], 12, v[84:85]
	v_lshl_add_u64 v[86:87], v[62:63], 0, v[86:87]
	v_lshl_add_u64 v[84:85], v[62:63], 0, v[84:85]
	global_load_dword v108, v[86:87], off
	global_load_dword v109, v[84:85], off
	v_mad_u64_u32 v[132:133], s[38:39], v89, s26, v[28:29]
	v_mad_u64_u32 v[134:135], s[38:39], v88, s26, v[28:29]
	v_add_u32_e32 v88, s37, v49
	v_add_u32_e32 v89, s36, v56
	v_add_u32_e32 v86, s36, v74
	v_add_u32_e32 v84, s37, v67
	v_ashrrev_i32_e32 v87, 31, v86
	v_ashrrev_i32_e32 v85, 31, v84
	v_lshlrev_b64 v[86:87], 12, v[86:87]
	v_lshlrev_b64 v[84:85], 12, v[84:85]
	v_lshl_add_u64 v[86:87], v[62:63], 0, v[86:87]
	v_lshl_add_u64 v[84:85], v[62:63], 0, v[84:85]
	global_load_dword v110, v[86:87], off
	global_load_dword v111, v[84:85], off
	v_mad_u64_u32 v[136:137], s[38:39], v89, s26, v[28:29]
	v_mad_u64_u32 v[138:139], s[38:39], v88, s26, v[28:29]
	v_add_u32_e32 v88, s37, v51
	v_add_u32_e32 v89, s36, v58
	v_add_u32_e32 v86, s36, v76
	v_add_u32_e32 v84, s37, v69
	v_ashrrev_i32_e32 v87, 31, v86
	v_ashrrev_i32_e32 v85, 31, v84
	v_lshlrev_b64 v[86:87], 12, v[86:87]
	v_lshlrev_b64 v[84:85], 12, v[84:85]
	v_lshl_add_u64 v[86:87], v[62:63], 0, v[86:87]
	v_lshl_add_u64 v[84:85], v[62:63], 0, v[84:85]
	global_load_dword v112, v[86:87], off
	global_load_dword v113, v[84:85], off
	v_mad_u64_u32 v[140:141], s[38:39], v89, s26, v[28:29]
	v_mad_u64_u32 v[142:143], s[38:39], v88, s26, v[28:29]
	v_add_u32_e32 v89, s36, v60
	v_add_u32_e32 v88, s37, v53
	v_add_u32_e32 v86, s36, v78
	v_add_u32_e32 v84, s37, v71
	v_ashrrev_i32_e32 v87, 31, v86
	v_ashrrev_i32_e32 v85, 31, v84
	v_lshlrev_b64 v[86:87], 12, v[86:87]
	v_lshlrev_b64 v[84:85], 12, v[84:85]
	v_lshl_add_u64 v[86:87], v[62:63], 0, v[86:87]
	v_lshl_add_u64 v[84:85], v[62:63], 0, v[84:85]
	global_load_dword v114, v[86:87], off
	global_load_dword v115, v[84:85], off
	v_mad_u64_u32 v[144:145], s[36:37], v89, s26, v[28:29]
	v_mad_u64_u32 v[146:147], s[36:37], v88, s26, v[28:29]
	s_waitcnt vmcnt(14)
	ds_write_b32 v116, v100
	ds_write_b32 v118, v101
	s_waitcnt vmcnt(12)
	ds_write_b32 v120, v102
	ds_write_b32 v122, v103
	s_waitcnt vmcnt(10)
	ds_write_b32 v124, v104
	ds_write_b32 v126, v105
	s_waitcnt vmcnt(8)
	ds_write_b32 v128, v106
	ds_write_b32 v130, v107
	s_waitcnt vmcnt(6)
	ds_write_b32 v132, v108
	ds_write_b32 v134, v109
	s_waitcnt vmcnt(4)
	ds_write_b32 v136, v110
	ds_write_b32 v138, v111
	s_waitcnt vmcnt(2)
	ds_write_b32 v140, v112
	ds_write_b32 v142, v113
	s_waitcnt vmcnt(0)
	ds_write_b32 v144, v114
	ds_write_b32 v146, v115
	s_cbranch_scc1 .LBB0_1224
; __device__ __forceinline__ unsigned cvt_pk_bf16(float lo, float hi) { unsigned r; asm volatile("v_cvt_pk_bf16_f32 %0, %1, %2" : "=v"(r) : "v"(lo), "v"(hi)); return r; }
; #define LAS __attribute__((address_space(3)))
;     ...
;     asm volatile("s_waitcnt lgkmcnt(0)" ::: "memory");
;     const int c = lane & 7;
; #pragma unroll
;     for (int j = 0; j < 4; ++j) { const int n = (lane >> 3) + 8 * j; const LAS float* s = scr + (8 * c) * 33 + n;
;         v4u o; o.x = cvt_pk_bf16(s[0 * 33], s[1 * 33]); o.y = cvt_pk_bf16(s[2 * 33], s[3 * 33]); o.z = cvt_pk_bf16(s[4 * 33], s[5 * 33]); o.w = cvt_pk_bf16(s[6 * 33], s[7 * 33]);
;         *(v4u*)(WT + (size_t)(row_off + n0 + n) * ldt + ((koff + k0 + 8 * c) ^ kx)) = o; }
;     asm volatile("s_waitcnt lgkmcnt(0)" ::: "memory");
	s_waitcnt lgkmcnt(0)
	ds_read2_b32 v[64:65], v77 offset1:33
	s_waitcnt lgkmcnt(0)
	v_cvt_pk_bf16_f32 v64, v64, v65
	ds_read2_b32 v[66:67], v77 offset0:66 offset1:99
	s_waitcnt lgkmcnt(0)
	v_cvt_pk_bf16_f32 v65, v66, v67
	ds_read2_b32 v[66:67], v77 offset0:132 offset1:165
	s_bitset1_b32 s5, 11
	s_waitcnt lgkmcnt(0)
	v_cvt_pk_bf16_f32 v66, v66, v67
	ds_read2_b32 v[68:69], v77 offset0:198 offset1:231
	v_or_b32_e32 v55, s0, v75
	s_waitcnt lgkmcnt(0)
	v_cvt_pk_bf16_f32 v67, v68, v69
	v_add_u32_e32 v68, s5, v30
	v_lshlrev_b32_e32 v62, 1, v55
	v_mov_b32_e32 v63, v0
	v_ashrrev_i32_e32 v69, 31, v68
	v_lshl_add_u64 v[62:63], s[42:43], 0, v[62:63]
	v_lshlrev_b64 v[68:69], 11, v[68:69]
	v_lshl_add_u64 v[68:69], v[62:63], 0, v[68:69]
	global_store_dwordx4 v[68:69], v[64:67], off
	ds_read2_b32 v[64:65], v77 offset0:8 offset1:41
	s_waitcnt lgkmcnt(0)
	v_cvt_pk_bf16_f32 v64, v64, v65
	ds_read2_b32 v[66:67], v77 offset0:74 offset1:107
	s_waitcnt lgkmcnt(0)
	v_cvt_pk_bf16_f32 v65, v66, v67
	ds_read2_b32 v[66:67], v77 offset0:140 offset1:173
	s_waitcnt lgkmcnt(0)
	v_cvt_pk_bf16_f32 v66, v66, v67
	ds_read2_b32 v[68:69], v77 offset0:206 offset1:239
	s_waitcnt lgkmcnt(0)
	v_cvt_pk_bf16_f32 v67, v68, v69
	v_add_u32_e32 v68, s5, v79
	v_ashrrev_i32_e32 v69, 31, v68
	v_lshlrev_b64 v[68:69], 11, v[68:69]
	v_lshl_add_u64 v[68:69], v[62:63], 0, v[68:69]
	global_store_dwordx4 v[68:69], v[64:67], off
	ds_read2_b32 v[64:65], v77 offset0:16 offset1:49
	s_waitcnt lgkmcnt(0)
	v_cvt_pk_bf16_f32 v64, v64, v65
	ds_read2_b32 v[66:67], v77 offset0:82 offset1:115
	s_waitcnt lgkmcnt(0)
	v_cvt_pk_bf16_f32 v65, v66, v67
	ds_read2_b32 v[66:67], v77 offset0:148 offset1:181
	s_waitcnt lgkmcnt(0)
	v_cvt_pk_bf16_f32 v66, v66, v67
	ds_read2_b32 v[68:69], v77 offset0:214 offset1:247
	s_waitcnt lgkmcnt(0)
	v_cvt_pk_bf16_f32 v67, v68, v69
	v_add_u32_e32 v68, s5, v80
	v_ashrrev_i32_e32 v69, 31, v68
	v_lshlrev_b64 v[68:69], 11, v[68:69]
	v_lshl_add_u64 v[68:69], v[62:63], 0, v[68:69]
	global_store_dwordx4 v[68:69], v[64:67], off
	ds_read2_b32 v[64:65], v77 offset0:24 offset1:57
	s_waitcnt lgkmcnt(0)
	v_cvt_pk_bf16_f32 v64, v64, v65
	ds_read2_b32 v[66:67], v77 offset0:90 offset1:123
	s_waitcnt lgkmcnt(0)
	v_cvt_pk_bf16_f32 v65, v66, v67
	ds_read2_b32 v[66:67], v77 offset0:156 offset1:189
	s_waitcnt lgkmcnt(0)
	v_cvt_pk_bf16_f32 v66, v66, v67
	ds_read2_b32 v[68:69], v77 offset0:222 offset1:255
	s_waitcnt lgkmcnt(0)
	v_cvt_pk_bf16_f32 v67, v68, v69
	v_add_u32_e32 v68, s5, v81
	v_ashrrev_i32_e32 v69, 31, v68
	v_lshlrev_b64 v[68:69], 11, v[68:69]
	v_lshl_add_u64 v[62:63], v[62:63], 0, v[68:69]
	global_store_dwordx4 v[62:63], v[64:67], off
	s_waitcnt lgkmcnt(0)

;     ...
; #pragma unroll 8
;     for (int i = 0; i < 32; ++i) { const int kk = 2 * i + (lane >> 5); scr[kk * 33 + (lane & 31)] = W[(size_t)(k0 + kk) * ldw + n0 + (lane & 31)]; }
.LBB0_1229:
	s_lshl_b32 s36, s23, 1
	s_lshl_b32 s37, s5, 1
	v_add_u32_e32 v86, s36, v64
	v_add_u32_e32 v84, s37, v55
	v_ashrrev_i32_e32 v87, 31, v86
	v_ashrrev_i32_e32 v85, 31, v84
	v_lshlrev_b64 v[86:87], 13, v[86:87]
	v_lshlrev_b64 v[84:85], 13, v[84:85]
	v_lshl_add_u64 v[86:87], v[62:63], 0, v[86:87]
	v_lshl_add_u64 v[84:85], v[62:63], 0, v[84:85]
	global_load_dword v100, v[86:87], off
	global_load_dword v101, v[84:85], off
	v_add_u32_e32 v88, s37, v1
	v_add_u32_e32 v89, s36, v26
	v_mad_u64_u32 v[116:117], s[38:39], v89, s26, v[28:29]
	v_mad_u64_u32 v[118:119], s[38:39], v88, s26, v[28:29]
	v_add_u32_e32 v88, s37, v3
	v_add_u32_e32 v89, s36, v48
	s_add_i32 s23, s23, 16
	s_add_i32 s5, s5, 16
	s_add_i32 s30, s30, -16
	s_cmp_lg_u32 s30, 0
	v_add_u32_e32 v86, s36, v66
	v_add_u32_e32 v84, s37, v57
	v_ashrrev_i32_e32 v87, 31, v86
	v_ashrrev_i32_e32 v85, 31, v84
	v_lshlrev_b64 v[86:87], 13, v[86:87]
	v_lshlrev_b64 v[84:85], 13, v[84:85]
	v_lshl_add_u64 v[86:87], v[62:63], 0, v[86:87]
	v_lshl_add_u64 v[84:85], v[62:63], 0, v[84:85]
	global_load_dword v102, v[86:87], off
	global_load_dword v103, v[84:85], off
	v_mad_u64_u32 v[120:121], s[38:39], v89, s26, v[28:29]
	v_mad_u64_u32 v[122:123], s[38:39], v88, s26, v[28:29]
	v_add_u32_e32 v88, s37, v27
	v_add_u32_e32 v89, s36, v50
	v_add_u32_e32 v86, s36, v68
	v_add_u32_e32 v84, s37, v59
	v_ashrrev_i32_e32 v87, 31, v86
	v_ashrrev_i32_e32 v85, 31, v84
	v_lshlrev_b64 v[86:87], 13, v[86:87]
	v_lshlrev_b64 v[84:85], 13, v[84:85]
	v_lshl_add_u64 v[86:87], v[62:63], 0, v[86:87]
	v_lshl_add_u64 v[84:85], v[62:63], 0, v[84:85]
	global_load_dword v104, v[86:87], off
	global_load_dword v105, v[84:85], off
	v_mad_u64_u32 v[124:125], s[38:39], v89, s26, v[28:29]
	v_mad_u64_u32 v[126:127], s[38:39], v88, s26, v[28:29]
	v_add_u32_e32 v88, s37, v29
	v_add_u32_e32 v89, s36, v52
	v_add_u32_e32 v86, s36, v70
	v_add_u32_e32 v84, s37, v61
	v_ashrrev_i32_e32 v87, 31, v86
	v_ashrrev_i32_e32 v85, 31, v84
	v_lshlrev_b64 v[86:87], 13, v[86:87]
	v_lshlrev_b64 v[84:85], 13, v[84:85]
	v_lshl_add_u64 v[86:87], v[62:63], 0, v[86:87]
	v_lshl_add_u64 v[84:85], v[62:63], 0, v[84:85]
	global_load_dword v106, v[86:87], off
	global_load_dword v107, v[84:85], off
	v_mad_u64_u32 v[128:129], s[38:39], v89, s26, v[28:29]
	v_mad_u64_u32 v[130:131], s[38:39], v88, s26, v[28:29]
	v_add_u32_e32 v88, s37, v31
	v_add_u32_e32 v89, s36, v54
	v_add_u32_e32 v86, s36, v72
	v_add_u32_e32 v84, s37, v65
	v_ashrrev_i32_e32 v87, 31, v86
	v_ashrrev_i32_e32 v85, 31, v84
	v_lshlrev_b64 v[86:87], 13, v[86:87]
	v_lshlrev_b64 v[84:85], 13, v[84:85]
	v_lshl_add_u64 v[86:87], v[62:63], 0, v[86:87]
	v_lshl_add_u64 v[84:85], v[62:63], 0, v[84:85]
	global_load_dword v108, v[86:87], off
	global_load_dword v109, v[84:85], off
	v_mad_u64_u32 v[132:133], s[38:39], v89, s26, v[28:29]
	v_mad_u64_u32 v[134:135], s[38:39], v88, s26, v[28:29]
	v_add_u32_e32 v88, s37, v49
	v_add_u32_e32 v89, s36, v56
	v_add_u32_e32 v86, s36, v74
	v_add_u32_e32 v84, s37, v67
	v_ashrrev_i32_e32 v87, 31, v86
	v_ashrrev_i32_e32 v85, 31, v84
	v_lshlrev_b64 v[86:87], 13, v[86:87]
	v_lshlrev_b64 v[84:85], 13, v[84:85]
	v_lshl_add_u64 v[86:87], v[62:63], 0, v[86:87]
	v_lshl_add_u64 v[84:85], v[62:63], 0, v[84:85]
	global_load_dword v110, v[86:87], off
	global_load_dword v111, v[84:85], off
	v_mad_u64_u32 v[136:137], s[38:39], v89, s26, v[28:29]
	v_mad_u64_u32 v[138:139], s[38:39], v88, s26, v[28:29]
	v_add_u32_e32 v88, s37, v51
	v_add_u32_e32 v89, s36, v58
	v_add_u32_e32 v86, s36, v76
	v_add_u32_e32 v84, s37, v69
	v_ashrrev_i32_e32 v87, 31, v86
	v_ashrrev_i32_e32 v85, 31, v84
	v_lshlrev_b64 v[86:87], 13, v[86:87]
	v_lshlrev_b64 v[84:85], 13, v[84:85]
	v_lshl_add_u64 v[86:87], v[62:63], 0, v[86:87]
	v_lshl_add_u64 v[84:85], v[62:63], 0, v[84:85]
	global_load_dword v112, v[86:87], off
	global_load_dword v113, v[84:85], off
	v_mad_u64_u32 v[140:141], s[38:39], v89, s26, v[28:29]
	v_mad_u64_u32 v[142:143], s[38:39], v88, s26, v[28:29]
	v_add_u32_e32 v89, s36, v60
	v_add_u32_e32 v88, s37, v53
	v_add_u32_e32 v86, s36, v78
	v_add_u32_e32 v84, s37, v71
	v_ashrrev_i32_e32 v87, 31, v86
	v_ashrrev_i32_e32 v85, 31, v84
	v_lshlrev_b64 v[86:87], 13, v[86:87]
	v_lshlrev_b64 v[84:85], 13, v[84:85]
	v_lshl_add_u64 v[86:87], v[62:63], 0, v[86:87]
	v_lshl_add_u64 v[84:85], v[62:63], 0, v[84:85]
	global_load_dword v114, v[86:87], off
	global_load_dword v115, v[84:85], off
	v_mad_u64_u32 v[144:145], s[36:37], v89, s26, v[28:29]
	v_mad_u64_u32 v[146:147], s[36:37], v88, s26, v[28:29]
	s_waitcnt vmcnt(14)
	ds_write_b32 v116, v100
	ds_write_b32 v118, v101
	s_waitcnt vmcnt(12)
	ds_write_b32 v120, v102
	ds_write_b32 v122, v103
	s_waitcnt vmcnt(10)
	ds_write_b32 v124, v104
	ds_write_b32 v126, v105
	s_waitcnt vmcnt(8)
	ds_write_b32 v128, v106
	ds_write_b32 v130, v107
	s_waitcnt vmcnt(6)
	ds_write_b32 v132, v108
	ds_write_b32 v134, v109
	s_waitcnt vmcnt(4)
	ds_write_b32 v136, v110
	ds_write_b32 v138, v111
	s_waitcnt vmcnt(2)
	ds_write_b32 v140, v112
	ds_write_b32 v142, v113
	s_waitcnt vmcnt(0)
	ds_write_b32 v144, v114
	ds_write_b32 v146, v115
	s_cbranch_scc1 .LBB0_1229
; __device__ __forceinline__ unsigned cvt_pk_bf16(float lo, float hi) { unsigned r; asm volatile("v_cvt_pk_bf16_f32 %0, %1, %2" : "=v"(r) : "v"(lo), "v"(hi)); return r; }
; #define LAS __attribute__((address_space(3)))
;     ...
;     asm volatile("s_waitcnt lgkmcnt(0)" ::: "memory");
;     const int c = lane & 7;
; #pragma unroll
;     for (int j = 0; j < 4; ++j) { const int n = (lane >> 3) + 8 * j; const LAS float* s = scr + (8 * c) * 33 + n;
;         v4u o; o.x = cvt_pk_bf16(s[0 * 33], s[1 * 33]); o.y = cvt_pk_bf16(s[2 * 33], s[3 * 33]); o.z = cvt_pk_bf16(s[4 * 33], s[5 * 33]); o.w = cvt_pk_bf16(s[6 * 33], s[7 * 33]);
;         *(v4u*)(WT + (size_t)(row_off + n0 + n) * ldt + ((koff + k0 + 8 * c) ^ kx)) = o; }
;     asm volatile("s_waitcnt lgkmcnt(0)" ::: "memory");
	s_waitcnt lgkmcnt(0)
	ds_read2_b32 v[64:65], v77 offset1:33
	s_waitcnt lgkmcnt(0)
	v_cvt_pk_bf16_f32 v64, v64, v65
	ds_read2_b32 v[66:67], v77 offset0:66 offset1:99
	s_waitcnt lgkmcnt(0)
	v_cvt_pk_bf16_f32 v65, v66, v67
	ds_read2_b32 v[66:67], v77 offset0:132 offset1:165
	s_waitcnt lgkmcnt(0)
	v_cvt_pk_bf16_f32 v66, v66, v67
	ds_read2_b32 v[68:69], v77 offset0:198 offset1:231
	v_or_b32_e32 v55, s1, v75
	s_waitcnt lgkmcnt(0)
	v_cvt_pk_bf16_f32 v67, v68, v69
	v_add_u32_e32 v68, s0, v30
	v_lshlrev_b32_e32 v62, 1, v55
	v_mov_b32_e32 v63, v0
	v_ashrrev_i32_e32 v69, 31, v68
	v_lshl_add_u64 v[62:63], s[42:43], 0, v[62:63]
	v_lshlrev_b64 v[68:69], 11, v[68:69]
	v_lshl_add_u64 v[68:69], v[62:63], 0, v[68:69]
	global_store_dwordx4 v[68:69], v[64:67], off
	ds_read2_b32 v[64:65], v77 offset0:8 offset1:41
	s_waitcnt lgkmcnt(0)
	v_cvt_pk_bf16_f32 v64, v64, v65
	ds_read2_b32 v[66:67], v77 offset0:74 offset1:107
	s_waitcnt lgkmcnt(0)
	v_cvt_pk_bf16_f32 v65, v66, v67
	ds_read2_b32 v[66:67], v77 offset0:140 offset1:173
	s_waitcnt lgkmcnt(0)
	v_cvt_pk_bf16_f32 v66, v66, v67
	ds_read2_b32 v[68:69], v77 offset0:206 offset1:239
	s_waitcnt lgkmcnt(0)
	v_cvt_pk_bf16_f32 v67, v68, v69
	v_add_u32_e32 v68, s0, v79
	v_ashrrev_i32_e32 v69, 31, v68
	v_lshlrev_b64 v[68:69], 11, v[68:69]
	v_lshl_add_u64 v[68:69], v[62:63], 0, v[68:69]
	global_store_dwordx4 v[68:69], v[64:67], off
	ds_read2_b32 v[64:65], v77 offset0:16 offset1:49
	s_waitcnt lgkmcnt(0)
	v_cvt_pk_bf16_f32 v64, v64, v65
	ds_read2_b32 v[66:67], v77 offset0:82 offset1:115
	s_waitcnt lgkmcnt(0)
	v_cvt_pk_bf16_f32 v65, v66, v67
	ds_read2_b32 v[66:67], v77 offset0:148 offset1:181
	s_waitcnt lgkmcnt(0)
	v_cvt_pk_bf16_f32 v66, v66, v67
	ds_read2_b32 v[68:69], v77 offset0:214 offset1:247
	s_waitcnt lgkmcnt(0)
	v_cvt_pk_bf16_f32 v67, v68, v69
	v_add_u32_e32 v68, s0, v80
	v_ashrrev_i32_e32 v69, 31, v68
	v_lshlrev_b64 v[68:69], 11, v[68:69]
	v_lshl_add_u64 v[68:69], v[62:63], 0, v[68:69]
	global_store_dwordx4 v[68:69], v[64:67], off
	ds_read2_b32 v[64:65], v77 offset0:24 offset1:57
	s_waitcnt lgkmcnt(0)
	v_cvt_pk_bf16_f32 v64, v64, v65
	ds_read2_b32 v[66:67], v77 offset0:90 offset1:123
	s_waitcnt lgkmcnt(0)
	v_cvt_pk_bf16_f32 v65, v66, v67
	ds_read2_b32 v[66:67], v77 offset0:156 offset1:189
	s_waitcnt lgkmcnt(0)
	v_cvt_pk_bf16_f32 v66, v66, v67
	ds_read2_b32 v[68:69], v77 offset0:222 offset1:255
	s_waitcnt lgkmcnt(0)
	v_cvt_pk_bf16_f32 v67, v68, v69
	v_add_u32_e32 v68, s0, v81
	v_ashrrev_i32_e32 v69, 31, v68
	v_lshlrev_b64 v[68:69], 11, v[68:69]
	v_lshl_add_u64 v[62:63], v[62:63], 0, v[68:69]
	global_store_dwordx4 v[62:63], v[64:67], off
	s_waitcnt lgkmcnt(0)

;     ...
; #pragma unroll 8
;     for (int i = 0; i < 32; ++i) { const int kk = 2 * i + (lane >> 5); scr[kk * 33 + (lane & 31)] = W[(size_t)(k0 + kk) * ldw + n0 + (lane & 31)]; }
.LBB0_1234:
	s_lshl_b32 s36, s23, 1
	s_lshl_b32 s37, s1, 1
	v_add_u32_e32 v86, s36, v64
	v_add_u32_e32 v84, s37, v55
	v_ashrrev_i32_e32 v87, 31, v86
	v_ashrrev_i32_e32 v85, 31, v84
	v_lshlrev_b64 v[86:87], 12, v[86:87]
	v_lshlrev_b64 v[84:85], 12, v[84:85]
	v_lshl_add_u64 v[86:87], v[62:63], 0, v[86:87]
	v_lshl_add_u64 v[84:85], v[62:63], 0, v[84:85]
	global_load_dword v100, v[86:87], off
	global_load_dword v101, v[84:85], off
	v_add_u32_e32 v88, s37, v1
	v_add_u32_e32 v89, s36, v26
	v_mad_u64_u32 v[116:117], s[38:39], v89, s26, v[28:29]
	v_mad_u64_u32 v[118:119], s[38:39], v88, s26, v[28:29]
	v_add_u32_e32 v88, s37, v3
	v_add_u32_e32 v89, s36, v48
	s_add_i32 s23, s23, 16
	s_add_i32 s1, s1, 16
	s_add_i32 s30, s30, -16
	s_cmp_lg_u32 s30, 0
	v_add_u32_e32 v86, s36, v66
	v_add_u32_e32 v84, s37, v57
	v_ashrrev_i32_e32 v87, 31, v86
	v_ashrrev_i32_e32 v85, 31, v84
	v_lshlrev_b64 v[86:87], 12, v[86:87]
	v_lshlrev_b64 v[84:85], 12, v[84:85]
	v_lshl_add_u64 v[86:87], v[62:63], 0, v[86:87]
	v_lshl_add_u64 v[84:85], v[62:63], 0, v[84:85]
	global_load_dword v102, v[86:87], off
	global_load_dword v103, v[84:85], off
	v_mad_u64_u32 v[120:121], s[38:39], v89, s26, v[28:29]
	v_mad_u64_u32 v[122:123], s[38:39], v88, s26, v[28:29]
	v_add_u32_e32 v88, s37, v27
	v_add_u32_e32 v89, s36, v50
	v_add_u32_e32 v86, s36, v68
	v_add_u32_e32 v84, s37, v59
	v_ashrrev_i32_e32 v87, 31, v86
	v_ashrrev_i32_e32 v85, 31, v84
	v_lshlrev_b64 v[86:87], 12, v[86:87]
	v_lshlrev_b64 v[84:85], 12, v[84:85]
	v_lshl_add_u64 v[86:87], v[62:63], 0, v[86:87]
	v_lshl_add_u64 v[84:85], v[62:63], 0, v[84:85]
	global_load_dword v104, v[86:87], off
	global_load_dword v105, v[84:85], off
	v_mad_u64_u32 v[124:125], s[38:39], v89, s26, v[28:29]
	v_mad_u64_u32 v[126:127], s[38:39], v88, s26, v[28:29]
	v_add_u32_e32 v88, s37, v29
	v_add_u32_e32 v89, s36, v52
	v_add_u32_e32 v86, s36, v70
	v_add_u32_e32 v84, s37, v61
	v_ashrrev_i32_e32 v87, 31, v86
	v_ashrrev_i32_e32 v85, 31, v84
	v_lshlrev_b64 v[86:87], 12, v[86:87]
	v_lshlrev_b64 v[84:85], 12, v[84:85]
	v_lshl_add_u64 v[86:87], v[62:63], 0, v[86:87]
	v_lshl_add_u64 v[84:85], v[62:63], 0, v[84:85]
	global_load_dword v106, v[86:87], off
	global_load_dword v107, v[84:85], off
	v_mad_u64_u32 v[128:129], s[38:39], v89, s26, v[28:29]
	v_mad_u64_u32 v[130:131], s[38:39], v88, s26, v[28:29]
	v_add_u32_e32 v88, s37, v31
	v_add_u32_e32 v89, s36, v54
	v_add_u32_e32 v86, s36, v72
	v_add_u32_e32 v84, s37, v65
	v_ashrrev_i32_e32 v87, 31, v86
	v_ashrrev_i32_e32 v85, 31, v84
	v_lshlrev_b64 v[86:87], 12, v[86:87]
	v_lshlrev_b64 v[84:85], 12, v[84:85]
	v_lshl_add_u64 v[86:87], v[62:63], 0, v[86:87]
	v_lshl_add_u64 v[84:85], v[62:63], 0, v[84:85]
	global_load_dword v108, v[86:87], off
	global_load_dword v109, v[84:85], off
	v_mad_u64_u32 v[132:133], s[38:39], v89, s26, v[28:29]
	v_mad_u64_u32 v[134:135], s[38:39], v88, s26, v[28:29]
	v_add_u32_e32 v88, s37, v49
	v_add_u32_e32 v89, s36, v56
	v_add_u32_e32 v86, s36, v74
	v_add_u32_e32 v84, s37, v67
	v_ashrrev_i32_e32 v87, 31, v86
	v_ashrrev_i32_e32 v85, 31, v84
	v_lshlrev_b64 v[86:87], 12, v[86:87]
	v_lshlrev_b64 v[84:85], 12, v[84:85]
	v_lshl_add_u64 v[86:87], v[62:63], 0, v[86:87]
	v_lshl_add_u64 v[84:85], v[62:63], 0, v[84:85]
	global_load_dword v110, v[86:87], off
	global_load_dword v111, v[84:85], off
	v_mad_u64_u32 v[136:137], s[38:39], v89, s26, v[28:29]
	v_mad_u64_u32 v[138:139], s[38:39], v88, s26, v[28:29]
	v_add_u32_e32 v88, s37, v51
	v_add_u32_e32 v89, s36, v58
	v_add_u32_e32 v86, s36, v76
	v_add_u32_e32 v84, s37, v69
	v_ashrrev_i32_e32 v87, 31, v86
	v_ashrrev_i32_e32 v85, 31, v84
	v_lshlrev_b64 v[86:87], 12, v[86:87]
	v_lshlrev_b64 v[84:85], 12, v[84:85]
	v_lshl_add_u64 v[86:87], v[62:63], 0, v[86:87]
	v_lshl_add_u64 v[84:85], v[62:63], 0, v[84:85]
	global_load_dword v112, v[86:87], off
	global_load_dword v113, v[84:85], off
	v_mad_u64_u32 v[140:141], s[38:39], v89, s26, v[28:29]
	v_mad_u64_u32 v[142:143], s[38:39], v88, s26, v[28:29]
	v_add_u32_e32 v89, s36, v60
	v_add_u32_e32 v88, s37, v53
	v_add_u32_e32 v86, s36, v78
	v_add_u32_e32 v84, s37, v71
	v_ashrrev_i32_e32 v87, 31, v86
	v_ashrrev_i32_e32 v85, 31, v84
	v_lshlrev_b64 v[86:87], 12, v[86:87]
	v_lshlrev_b64 v[84:85], 12, v[84:85]
	v_lshl_add_u64 v[86:87], v[62:63], 0, v[86:87]
	v_lshl_add_u64 v[84:85], v[62:63], 0, v[84:85]
	global_load_dword v114, v[86:87], off
	global_load_dword v115, v[84:85], off
	v_mad_u64_u32 v[144:145], s[36:37], v89, s26, v[28:29]
	v_mad_u64_u32 v[146:147], s[36:37], v88, s26, v[28:29]
	s_waitcnt vmcnt(14)
	ds_write_b32 v116, v100
	ds_write_b32 v118, v101
	s_waitcnt vmcnt(12)
	ds_write_b32 v120, v102
	ds_write_b32 v122, v103
	s_waitcnt vmcnt(10)
	ds_write_b32 v124, v104
	ds_write_b32 v126, v105
	s_waitcnt vmcnt(8)
	ds_write_b32 v128, v106
	ds_write_b32 v130, v107
	s_waitcnt vmcnt(6)
	ds_write_b32 v132, v108
	ds_write_b32 v134, v109
	s_waitcnt vmcnt(4)
	ds_write_b32 v136, v110
	ds_write_b32 v138, v111
	s_waitcnt vmcnt(2)
	ds_write_b32 v140, v112
	ds_write_b32 v142, v113
	s_waitcnt vmcnt(0)
	ds_write_b32 v144, v114
	ds_write_b32 v146, v115
	s_cbranch_scc1 .LBB0_1234
; __device__ __forceinline__ unsigned cvt_pk_bf16(float lo, float hi) { unsigned r; asm volatile("v_cvt_pk_bf16_f32 %0, %1, %2" : "=v"(r) : "v"(lo), "v"(hi)); return r; }
; #define LAS __attribute__((address_space(3)))
;     ...
;     asm volatile("s_waitcnt lgkmcnt(0)" ::: "memory");
;     const int c = lane & 7;
; #pragma unroll
;     for (int j = 0; j < 4; ++j) { const int n = (lane >> 3) + 8 * j; const LAS float* s = scr + (8 * c) * 33 + n;
;         v4u o; o.x = cvt_pk_bf16(s[0 * 33], s[1 * 33]); o.y = cvt_pk_bf16(s[2 * 33], s[3 * 33]); o.z = cvt_pk_bf16(s[4 * 33], s[5 * 33]); o.w = cvt_pk_bf16(s[6 * 33], s[7 * 33]);
;         *(v4u*)(WT + (size_t)(row_off + n0 + n) * ldt + ((koff + k0 + 8 * c) ^ kx)) = o; }
;     asm volatile("s_waitcnt lgkmcnt(0)" ::: "memory");
	s_waitcnt lgkmcnt(0)
	ds_read2_b32 v[64:65], v77 offset1:33
	s_waitcnt lgkmcnt(0)
	v_cvt_pk_bf16_f32 v64, v64, v65
	ds_read2_b32 v[66:67], v77 offset0:66 offset1:99
	s_waitcnt lgkmcnt(0)
	v_cvt_pk_bf16_f32 v65, v66, v67
	ds_read2_b32 v[66:67], v77 offset0:132 offset1:165
	s_waitcnt lgkmcnt(0)
	v_cvt_pk_bf16_f32 v66, v66, v67
	ds_read2_b32 v[68:69], v77 offset0:198 offset1:231
	v_or_b32_e32 v55, s5, v75
	s_waitcnt lgkmcnt(0)
	v_cvt_pk_bf16_f32 v67, v68, v69
	v_add_u32_e32 v68, s0, v30
	v_lshlrev_b32_e32 v62, 1, v55
	v_mov_b32_e32 v63, v0
	v_ashrrev_i32_e32 v69, 31, v68
	v_lshl_add_u64 v[62:63], s[44:45], 0, v[62:63]
	v_lshlrev_b64 v[68:69], 11, v[68:69]
	v_lshl_add_u64 v[68:69], v[62:63], 0, v[68:69]
	global_store_dwordx4 v[68:69], v[64:67], off
	ds_read2_b32 v[64:65], v77 offset0:8 offset1:41
	s_waitcnt lgkmcnt(0)
	v_cvt_pk_bf16_f32 v64, v64, v65
	ds_read2_b32 v[66:67], v77 offset0:74 offset1:107
	s_waitcnt lgkmcnt(0)
	v_cvt_pk_bf16_f32 v65, v66, v67
	ds_read2_b32 v[66:67], v77 offset0:140 offset1:173
	s_waitcnt lgkmcnt(0)
	v_cvt_pk_bf16_f32 v66, v66, v67
	ds_read2_b32 v[68:69], v77 offset0:206 offset1:239
	s_waitcnt lgkmcnt(0)
	v_cvt_pk_bf16_f32 v67, v68, v69
	v_add_u32_e32 v68, s0, v79
	v_ashrrev_i32_e32 v69, 31, v68
	v_lshlrev_b64 v[68:69], 11, v[68:69]
	v_lshl_add_u64 v[68:69], v[62:63], 0, v[68:69]
	global_store_dwordx4 v[68:69], v[64:67], off
	ds_read2_b32 v[64:65], v77 offset0:16 offset1:49
	s_waitcnt lgkmcnt(0)
	v_cvt_pk_bf16_f32 v64, v64, v65
	ds_read2_b32 v[66:67], v77 offset0:82 offset1:115
	s_waitcnt lgkmcnt(0)
	v_cvt_pk_bf16_f32 v65, v66, v67
	ds_read2_b32 v[66:67], v77 offset0:148 offset1:181
	s_waitcnt lgkmcnt(0)
	v_cvt_pk_bf16_f32 v66, v66, v67
	ds_read2_b32 v[68:69], v77 offset0:214 offset1:247
	s_waitcnt lgkmcnt(0)
	v_cvt_pk_bf16_f32 v67, v68, v69
	v_add_u32_e32 v68, s0, v80
	v_ashrrev_i32_e32 v69, 31, v68
	v_lshlrev_b64 v[68:69], 11, v[68:69]
	v_lshl_add_u64 v[68:69], v[62:63], 0, v[68:69]
	global_store_dwordx4 v[68:69], v[64:67], off
	ds_read2_b32 v[64:65], v77 offset0:24 offset1:57
	s_waitcnt lgkmcnt(0)
	v_cvt_pk_bf16_f32 v64, v64, v65
	ds_read2_b32 v[66:67], v77 offset0:90 offset1:123
	s_waitcnt lgkmcnt(0)
	v_cvt_pk_bf16_f32 v65, v66, v67
	ds_read2_b32 v[66:67], v77 offset0:156 offset1:189
	s_waitcnt lgkmcnt(0)
	v_cvt_pk_bf16_f32 v66, v66, v67
	ds_read2_b32 v[68:69], v77 offset0:222 offset1:255
	s_waitcnt lgkmcnt(0)
	v_cvt_pk_bf16_f32 v67, v68, v69
	v_add_u32_e32 v68, s0, v81
	v_ashrrev_i32_e32 v69, 31, v68
	v_lshlrev_b64 v[68:69], 11, v[68:69]
	v_lshl_add_u64 v[62:63], v[62:63], 0, v[68:69]
	global_store_dwordx4 v[62:63], v[64:67], off
	s_waitcnt lgkmcnt(0)

;     ...
; #pragma unroll 8
;     for (int i = 0; i < 32; ++i) { const int kk = 2 * i + (lane >> 5); scr[kk * 33 + (lane & 31)] = W[(size_t)(k0 + kk) * ldw + n0 + (lane & 31)]; }
.LBB0_1239:
	s_lshl_b32 s36, s23, 1
	s_lshl_b32 s37, s1, 1
	v_add_u32_e32 v86, s36, v64
	v_add_u32_e32 v84, s37, v55
	v_ashrrev_i32_e32 v87, 31, v86
	v_ashrrev_i32_e32 v85, 31, v84
	v_lshlrev_b64 v[86:87], 12, v[86:87]
	v_lshlrev_b64 v[84:85], 12, v[84:85]
	v_lshl_add_u64 v[86:87], v[62:63], 0, v[86:87]
	v_lshl_add_u64 v[84:85], v[62:63], 0, v[84:85]
	global_load_dword v100, v[86:87], off
	global_load_dword v101, v[84:85], off
	v_add_u32_e32 v88, s37, v1
	v_add_u32_e32 v89, s36, v26
	v_mad_u64_u32 v[116:117], s[38:39], v89, s26, v[28:29]
	v_mad_u64_u32 v[118:119], s[38:39], v88, s26, v[28:29]
	v_add_u32_e32 v88, s37, v3
	v_add_u32_e32 v89, s36, v48
	s_add_i32 s23, s23, 16
	s_add_i32 s1, s1, 16
	s_add_i32 s30, s30, -16
	s_cmp_lg_u32 s30, 0
	v_add_u32_e32 v86, s36, v66
	v_add_u32_e32 v84, s37, v57
	v_ashrrev_i32_e32 v87, 31, v86
	v_ashrrev_i32_e32 v85, 31, v84
	v_lshlrev_b64 v[86:87], 12, v[86:87]
	v_lshlrev_b64 v[84:85], 12, v[84:85]
	v_lshl_add_u64 v[86:87], v[62:63], 0, v[86:87]
	v_lshl_add_u64 v[84:85], v[62:63], 0, v[84:85]
	global_load_dword v102, v[86:87], off
	global_load_dword v103, v[84:85], off
	v_mad_u64_u32 v[120:121], s[38:39], v89, s26, v[28:29]
	v_mad_u64_u32 v[122:123], s[38:39], v88, s26, v[28:29]
	v_add_u32_e32 v88, s37, v27
	v_add_u32_e32 v89, s36, v50
	v_add_u32_e32 v86, s36, v68
	v_add_u32_e32 v84, s37, v59
	v_ashrrev_i32_e32 v87, 31, v86
	v_ashrrev_i32_e32 v85, 31, v84
	v_lshlrev_b64 v[86:87], 12, v[86:87]
	v_lshlrev_b64 v[84:85], 12, v[84:85]
	v_lshl_add_u64 v[86:87], v[62:63], 0, v[86:87]
	v_lshl_add_u64 v[84:85], v[62:63], 0, v[84:85]
	global_load_dword v104, v[86:87], off
	global_load_dword v105, v[84:85], off
	v_mad_u64_u32 v[124:125], s[38:39], v89, s26, v[28:29]
	v_mad_u64_u32 v[126:127], s[38:39], v88, s26, v[28:29]
	v_add_u32_e32 v88, s37, v29
	v_add_u32_e32 v89, s36, v52
	v_add_u32_e32 v86, s36, v70
	v_add_u32_e32 v84, s37, v61
	v_ashrrev_i32_e32 v87, 31, v86
	v_ashrrev_i32_e32 v85, 31, v84
	v_lshlrev_b64 v[86:87], 12, v[86:87]
	v_lshlrev_b64 v[84:85], 12, v[84:85]
	v_lshl_add_u64 v[86:87], v[62:63], 0, v[86:87]
	v_lshl_add_u64 v[84:85], v[62:63], 0, v[84:85]
	global_load_dword v106, v[86:87], off
	global_load_dword v107, v[84:85], off
	v_mad_u64_u32 v[128:129], s[38:39], v89, s26, v[28:29]
	v_mad_u64_u32 v[130:131], s[38:39], v88, s26, v[28:29]
	v_add_u32_e32 v88, s37, v31
	v_add_u32_e32 v89, s36, v54
	v_add_u32_e32 v86, s36, v72
	v_add_u32_e32 v84, s37, v65
	v_ashrrev_i32_e32 v87, 31, v86
	v_ashrrev_i32_e32 v85, 31, v84
	v_lshlrev_b64 v[86:87], 12, v[86:87]
	v_lshlrev_b64 v[84:85], 12, v[84:85]
	v_lshl_add_u64 v[86:87], v[62:63], 0, v[86:87]
	v_lshl_add_u64 v[84:85], v[62:63], 0, v[84:85]
	global_load_dword v108, v[86:87], off
	global_load_dword v109, v[84:85], off
	v_mad_u64_u32 v[132:133], s[38:39], v89, s26, v[28:29]
	v_mad_u64_u32 v[134:135], s[38:39], v88, s26, v[28:29]
	v_add_u32_e32 v88, s37, v49
	v_add_u32_e32 v89, s36, v56
	v_add_u32_e32 v86, s36, v74
	v_add_u32_e32 v84, s37, v67
	v_ashrrev_i32_e32 v87, 31, v86
	v_ashrrev_i32_e32 v85, 31, v84
	v_lshlrev_b64 v[86:87], 12, v[86:87]
	v_lshlrev_b64 v[84:85], 12, v[84:85]
	v_lshl_add_u64 v[86:87], v[62:63], 0, v[86:87]
	v_lshl_add_u64 v[84:85], v[62:63], 0, v[84:85]
	global_load_dword v110, v[86:87], off
	global_load_dword v111, v[84:85], off
	v_mad_u64_u32 v[136:137], s[38:39], v89, s26, v[28:29]
	v_mad_u64_u32 v[138:139], s[38:39], v88, s26, v[28:29]
	v_add_u32_e32 v88, s37, v51
	v_add_u32_e32 v89, s36, v58
	v_add_u32_e32 v86, s36, v76
	v_add_u32_e32 v84, s37, v69
	v_ashrrev_i32_e32 v87, 31, v86
	v_ashrrev_i32_e32 v85, 31, v84
	v_lshlrev_b64 v[86:87], 12, v[86:87]
	v_lshlrev_b64 v[84:85], 12, v[84:85]
	v_lshl_add_u64 v[86:87], v[62:63], 0, v[86:87]
	v_lshl_add_u64 v[84:85], v[62:63], 0, v[84:85]
	global_load_dword v112, v[86:87], off
	global_load_dword v113, v[84:85], off
	v_mad_u64_u32 v[140:141], s[38:39], v89, s26, v[28:29]
	v_mad_u64_u32 v[142:143], s[38:39], v88, s26, v[28:29]
	v_add_u32_e32 v89, s36, v60
	v_add_u32_e32 v88, s37, v53
	v_add_u32_e32 v86, s36, v78
	v_add_u32_e32 v84, s37, v71
	v_ashrrev_i32_e32 v87, 31, v86
	v_ashrrev_i32_e32 v85, 31, v84
	v_lshlrev_b64 v[86:87], 12, v[86:87]
	v_lshlrev_b64 v[84:85], 12, v[84:85]
	v_lshl_add_u64 v[86:87], v[62:63], 0, v[86:87]
	v_lshl_add_u64 v[84:85], v[62:63], 0, v[84:85]
	global_load_dword v114, v[86:87], off
	global_load_dword v115, v[84:85], off
	v_mad_u64_u32 v[144:145], s[36:37], v89, s26, v[28:29]
	v_mad_u64_u32 v[146:147], s[36:37], v88, s26, v[28:29]
	s_waitcnt vmcnt(14)
	ds_write_b32 v116, v100
	ds_write_b32 v118, v101
	s_waitcnt vmcnt(12)
	ds_write_b32 v120, v102
	ds_write_b32 v122, v103
	s_waitcnt vmcnt(10)
	ds_write_b32 v124, v104
	ds_write_b32 v126, v105
	s_waitcnt vmcnt(8)
	ds_write_b32 v128, v106
	ds_write_b32 v130, v107
	s_waitcnt vmcnt(6)
	ds_write_b32 v132, v108
	ds_write_b32 v134, v109
	s_waitcnt vmcnt(4)
	ds_write_b32 v136, v110
	ds_write_b32 v138, v111
	s_waitcnt vmcnt(2)
	ds_write_b32 v140, v112
	ds_write_b32 v142, v113
	s_waitcnt vmcnt(0)
	ds_write_b32 v144, v114
	ds_write_b32 v146, v115
	s_cbranch_scc1 .LBB0_1239
; __device__ __forceinline__ unsigned cvt_pk_bf16(float lo, float hi) { unsigned r; asm volatile("v_cvt_pk_bf16_f32 %0, %1, %2" : "=v"(r) : "v"(lo), "v"(hi)); return r; }
; #define LAS __attribute__((address_space(3)))
;     ...
;     asm volatile("s_waitcnt lgkmcnt(0)" ::: "memory");
;     const int c = lane & 7;
; #pragma unroll
;     for (int j = 0; j < 4; ++j) { const int n = (lane >> 3) + 8 * j; const LAS float* s = scr + (8 * c) * 33 + n;
;         v4u o; o.x = cvt_pk_bf16(s[0 * 33], s[1 * 33]); o.y = cvt_pk_bf16(s[2 * 33], s[3 * 33]); o.z = cvt_pk_bf16(s[4 * 33], s[5 * 33]); o.w = cvt_pk_bf16(s[6 * 33], s[7 * 33]);
;         *(v4u*)(WT + (size_t)(row_off + n0 + n) * ldt + ((koff + k0 + 8 * c) ^ kx)) = o; }
;     asm volatile("s_waitcnt lgkmcnt(0)" ::: "memory");
	s_waitcnt lgkmcnt(0)
	ds_read2_b32 v[64:65], v77 offset1:33
	s_waitcnt lgkmcnt(0)
	v_cvt_pk_bf16_f32 v64, v64, v65
	ds_read2_b32 v[66:67], v77 offset0:66 offset1:99
	s_waitcnt lgkmcnt(0)
	v_cvt_pk_bf16_f32 v65, v66, v67
	ds_read2_b32 v[66:67], v77 offset0:132 offset1:165
	s_waitcnt lgkmcnt(0)
	v_cvt_pk_bf16_f32 v66, v66, v67
	ds_read2_b32 v[68:69], v77 offset0:198 offset1:231
	v_or_b32_e32 v55, s5, v75
	s_waitcnt lgkmcnt(0)
	v_cvt_pk_bf16_f32 v67, v68, v69
	v_add_u32_e32 v68, s0, v30
	v_lshlrev_b32_e32 v62, 1, v55
	v_mov_b32_e32 v63, v0
	v_ashrrev_i32_e32 v69, 31, v68
	v_lshl_add_u64 v[62:63], s[46:47], 0, v[62:63]
	v_lshlrev_b64 v[68:69], 11, v[68:69]
	v_lshl_add_u64 v[68:69], v[62:63], 0, v[68:69]
	global_store_dwordx4 v[68:69], v[64:67], off
	ds_read2_b32 v[64:65], v77 offset0:8 offset1:41
	s_waitcnt lgkmcnt(0)
	v_cvt_pk_bf16_f32 v64, v64, v65
	ds_read2_b32 v[66:67], v77 offset0:74 offset1:107
	s_waitcnt lgkmcnt(0)
	v_cvt_pk_bf16_f32 v65, v66, v67
	ds_read2_b32 v[66:67], v77 offset0:140 offset1:173
	s_waitcnt lgkmcnt(0)
	v_cvt_pk_bf16_f32 v66, v66, v67
	ds_read2_b32 v[68:69], v77 offset0:206 offset1:239
	s_waitcnt lgkmcnt(0)
	v_cvt_pk_bf16_f32 v67, v68, v69
	v_add_u32_e32 v68, s0, v79
	v_ashrrev_i32_e32 v69, 31, v68
	v_lshlrev_b64 v[68:69], 11, v[68:69]
	v_lshl_add_u64 v[68:69], v[62:63], 0, v[68:69]
	global_store_dwordx4 v[68:69], v[64:67], off
	ds_read2_b32 v[64:65], v77 offset0:16 offset1:49
	s_waitcnt lgkmcnt(0)
	v_cvt_pk_bf16_f32 v64, v64, v65
	ds_read2_b32 v[66:67], v77 offset0:82 offset1:115
	s_waitcnt lgkmcnt(0)
	v_cvt_pk_bf16_f32 v65, v66, v67
	ds_read2_b32 v[66:67], v77 offset0:148 offset1:181
	s_waitcnt lgkmcnt(0)
	v_cvt_pk_bf16_f32 v66, v66, v67
	ds_read2_b32 v[68:69], v77 offset0:214 offset1:247
	s_waitcnt lgkmcnt(0)
	v_cvt_pk_bf16_f32 v67, v68, v69
	v_add_u32_e32 v68, s0, v80
	v_ashrrev_i32_e32 v69, 31, v68
	v_lshlrev_b64 v[68:69], 11, v[68:69]
	v_lshl_add_u64 v[68:69], v[62:63], 0, v[68:69]
	global_store_dwordx4 v[68:69], v[64:67], off
	ds_read2_b32 v[64:65], v77 offset0:24 offset1:57
	s_waitcnt lgkmcnt(0)
	v_cvt_pk_bf16_f32 v64, v64, v65
	ds_read2_b32 v[66:67], v77 offset0:90 offset1:123
	s_waitcnt lgkmcnt(0)
	v_cvt_pk_bf16_f32 v65, v66, v67
	ds_read2_b32 v[66:67], v77 offset0:156 offset1:189
	s_waitcnt lgkmcnt(0)
	v_cvt_pk_bf16_f32 v66, v66, v67
	ds_read2_b32 v[68:69], v77 offset0:222 offset1:255
	s_waitcnt lgkmcnt(0)
	v_cvt_pk_bf16_f32 v67, v68, v69
	v_add_u32_e32 v68, s0, v81
	v_ashrrev_i32_e32 v69, 31, v68
	v_lshlrev_b64 v[68:69], 11, v[68:69]
	v_lshl_add_u64 v[62:63], v[62:63], 0, v[68:69]
	global_store_dwordx4 v[62:63], v[64:67], off
	s_waitcnt lgkmcnt(0)

;     ...
; #pragma unroll 8
;     for (int i = 0; i < 32; ++i) { const int kk = 2 * i + (lane >> 5); scr[kk * 33 + (lane & 31)] = W[(size_t)(k0 + kk) * ldw + n0 + (lane & 31)]; }
.LBB0_1244:
	s_lshl_b32 s36, s23, 1
	s_lshl_b32 s37, s1, 1
	v_add_u32_e32 v86, s36, v64
	v_add_u32_e32 v84, s37, v55
	v_ashrrev_i32_e32 v87, 31, v86
	v_ashrrev_i32_e32 v85, 31, v84
	v_lshlrev_b64 v[86:87], 12, v[86:87]
	v_lshlrev_b64 v[84:85], 12, v[84:85]
	v_lshl_add_u64 v[86:87], v[62:63], 0, v[86:87]
	v_lshl_add_u64 v[84:85], v[62:63], 0, v[84:85]
	global_load_dword v100, v[86:87], off
	global_load_dword v101, v[84:85], off
	v_add_u32_e32 v88, s37, v1
	v_add_u32_e32 v89, s36, v26
	v_mad_u64_u32 v[116:117], s[38:39], v89, s26, v[28:29]
	v_mad_u64_u32 v[118:119], s[38:39], v88, s26, v[28:29]
	v_add_u32_e32 v88, s37, v3
	v_add_u32_e32 v89, s36, v48
	s_add_i32 s23, s23, 16
	s_add_i32 s1, s1, 16
	s_add_i32 s30, s30, -16
	s_cmp_lg_u32 s30, 0
	v_add_u32_e32 v86, s36, v66
	v_add_u32_e32 v84, s37, v57
	v_ashrrev_i32_e32 v87, 31, v86
	v_ashrrev_i32_e32 v85, 31, v84
	v_lshlrev_b64 v[86:87], 12, v[86:87]
	v_lshlrev_b64 v[84:85], 12, v[84:85]
	v_lshl_add_u64 v[86:87], v[62:63], 0, v[86:87]
	v_lshl_add_u64 v[84:85], v[62:63], 0, v[84:85]
	global_load_dword v102, v[86:87], off
	global_load_dword v103, v[84:85], off
	v_mad_u64_u32 v[120:121], s[38:39], v89, s26, v[28:29]
	v_mad_u64_u32 v[122:123], s[38:39], v88, s26, v[28:29]
	v_add_u32_e32 v88, s37, v27
	v_add_u32_e32 v89, s36, v50
	v_add_u32_e32 v86, s36, v68
	v_add_u32_e32 v84, s37, v59
	v_ashrrev_i32_e32 v87, 31, v86
	v_ashrrev_i32_e32 v85, 31, v84
	v_lshlrev_b64 v[86:87], 12, v[86:87]
	v_lshlrev_b64 v[84:85], 12, v[84:85]
	v_lshl_add_u64 v[86:87], v[62:63], 0, v[86:87]
	v_lshl_add_u64 v[84:85], v[62:63], 0, v[84:85]
	global_load_dword v104, v[86:87], off
	global_load_dword v105, v[84:85], off
	v_mad_u64_u32 v[124:125], s[38:39], v89, s26, v[28:29]
	v_mad_u64_u32 v[126:127], s[38:39], v88, s26, v[28:29]
	v_add_u32_e32 v88, s37, v29
	v_add_u32_e32 v89, s36, v52
	v_add_u32_e32 v86, s36, v70
	v_add_u32_e32 v84, s37, v61
	v_ashrrev_i32_e32 v87, 31, v86
	v_ashrrev_i32_e32 v85, 31, v84
	v_lshlrev_b64 v[86:87], 12, v[86:87]
	v_lshlrev_b64 v[84:85], 12, v[84:85]
	v_lshl_add_u64 v[86:87], v[62:63], 0, v[86:87]
	v_lshl_add_u64 v[84:85], v[62:63], 0, v[84:85]
	global_load_dword v106, v[86:87], off
	global_load_dword v107, v[84:85], off
	v_mad_u64_u32 v[128:129], s[38:39], v89, s26, v[28:29]
	v_mad_u64_u32 v[130:131], s[38:39], v88, s26, v[28:29]
	v_add_u32_e32 v88, s37, v31
	v_add_u32_e32 v89, s36, v54
	v_add_u32_e32 v86, s36, v72
	v_add_u32_e32 v84, s37, v65
	v_ashrrev_i32_e32 v87, 31, v86
	v_ashrrev_i32_e32 v85, 31, v84
	v_lshlrev_b64 v[86:87], 12, v[86:87]
	v_lshlrev_b64 v[84:85], 12, v[84:85]
	v_lshl_add_u64 v[86:87], v[62:63], 0, v[86:87]
	v_lshl_add_u64 v[84:85], v[62:63], 0, v[84:85]
	global_load_dword v108, v[86:87], off
	global_load_dword v109, v[84:85], off
	v_mad_u64_u32 v[132:133], s[38:39], v89, s26, v[28:29]
	v_mad_u64_u32 v[134:135], s[38:39], v88, s26, v[28:29]
	v_add_u32_e32 v88, s37, v49
	v_add_u32_e32 v89, s36, v56
	v_add_u32_e32 v86, s36, v74
	v_add_u32_e32 v84, s37, v67
	v_ashrrev_i32_e32 v87, 31, v86
	v_ashrrev_i32_e32 v85, 31, v84
	v_lshlrev_b64 v[86:87], 12, v[86:87]
	v_lshlrev_b64 v[84:85], 12, v[84:85]
	v_lshl_add_u64 v[86:87], v[62:63], 0, v[86:87]
	v_lshl_add_u64 v[84:85], v[62:63], 0, v[84:85]
	global_load_dword v110, v[86:87], off
	global_load_dword v111, v[84:85], off
	v_mad_u64_u32 v[136:137], s[38:39], v89, s26, v[28:29]
	v_mad_u64_u32 v[138:139], s[38:39], v88, s26, v[28:29]
	v_add_u32_e32 v88, s37, v51
	v_add_u32_e32 v89, s36, v58
	v_add_u32_e32 v86, s36, v76
	v_add_u32_e32 v84, s37, v69
	v_ashrrev_i32_e32 v87, 31, v86
	v_ashrrev_i32_e32 v85, 31, v84
	v_lshlrev_b64 v[86:87], 12, v[86:87]
	v_lshlrev_b64 v[84:85], 12, v[84:85]
	v_lshl_add_u64 v[86:87], v[62:63], 0, v[86:87]
	v_lshl_add_u64 v[84:85], v[62:63], 0, v[84:85]
	global_load_dword v112, v[86:87], off
	global_load_dword v113, v[84:85], off
	v_mad_u64_u32 v[140:141], s[38:39], v89, s26, v[28:29]
	v_mad_u64_u32 v[142:143], s[38:39], v88, s26, v[28:29]
	v_add_u32_e32 v89, s36, v60
	v_add_u32_e32 v88, s37, v53
	v_add_u32_e32 v86, s36, v78
	v_add_u32_e32 v84, s37, v71
	v_ashrrev_i32_e32 v87, 31, v86
	v_ashrrev_i32_e32 v85, 31, v84
	v_lshlrev_b64 v[86:87], 12, v[86:87]
	v_lshlrev_b64 v[84:85], 12, v[84:85]
	v_lshl_add_u64 v[86:87], v[62:63], 0, v[86:87]
	v_lshl_add_u64 v[84:85], v[62:63], 0, v[84:85]
	global_load_dword v114, v[86:87], off
	global_load_dword v115, v[84:85], off
	v_mad_u64_u32 v[144:145], s[36:37], v89, s26, v[28:29]
	v_mad_u64_u32 v[146:147], s[36:37], v88, s26, v[28:29]
	s_waitcnt vmcnt(14)
	ds_write_b32 v116, v100
	ds_write_b32 v118, v101
	s_waitcnt vmcnt(12)
	ds_write_b32 v120, v102
	ds_write_b32 v122, v103
	s_waitcnt vmcnt(10)
	ds_write_b32 v124, v104
	ds_write_b32 v126, v105
	s_waitcnt vmcnt(8)
	ds_write_b32 v128, v106
	ds_write_b32 v130, v107
	s_waitcnt vmcnt(6)
	ds_write_b32 v132, v108
	ds_write_b32 v134, v109
	s_waitcnt vmcnt(4)
	ds_write_b32 v136, v110
	ds_write_b32 v138, v111
	s_waitcnt vmcnt(2)
	ds_write_b32 v140, v112
	ds_write_b32 v142, v113
	s_waitcnt vmcnt(0)
	ds_write_b32 v144, v114
	ds_write_b32 v146, v115
	s_cbranch_scc1 .LBB0_1244
; __device__ __forceinline__ unsigned cvt_pk_bf16(float lo, float hi) { unsigned r; asm volatile("v_cvt_pk_bf16_f32 %0, %1, %2" : "=v"(r) : "v"(lo), "v"(hi)); return r; }
; #define LAS __attribute__((address_space(3)))
;     ...
;     asm volatile("s_waitcnt lgkmcnt(0)" ::: "memory");
;     const int c = lane & 7;
; #pragma unroll
;     for (int j = 0; j < 4; ++j) { const int n = (lane >> 3) + 8 * j; const LAS float* s = scr + (8 * c) * 33 + n;
;         v4u o; o.x = cvt_pk_bf16(s[0 * 33], s[1 * 33]); o.y = cvt_pk_bf16(s[2 * 33], s[3 * 33]); o.z = cvt_pk_bf16(s[4 * 33], s[5 * 33]); o.w = cvt_pk_bf16(s[6 * 33], s[7 * 33]);
;         *(v4u*)(WT + (size_t)(row_off + n0 + n) * ldt + ((koff + k0 + 8 * c) ^ kx)) = o; }
;     asm volatile("s_waitcnt lgkmcnt(0)" ::: "memory");
	s_waitcnt lgkmcnt(0)
	ds_read2_b32 v[64:65], v77 offset1:33
	s_waitcnt lgkmcnt(0)
	v_cvt_pk_bf16_f32 v64, v64, v65
	ds_read2_b32 v[66:67], v77 offset0:66 offset1:99
	s_waitcnt lgkmcnt(0)
	v_cvt_pk_bf16_f32 v65, v66, v67
	ds_read2_b32 v[66:67], v77 offset0:132 offset1:165
	s_waitcnt lgkmcnt(0)
	v_cvt_pk_bf16_f32 v66, v66, v67
	ds_read2_b32 v[68:69], v77 offset0:198 offset1:231
	v_or_b32_e32 v55, s5, v75
	s_waitcnt lgkmcnt(0)
	v_cvt_pk_bf16_f32 v67, v68, v69
	v_add_u32_e32 v68, s0, v30
	v_lshlrev_b32_e32 v62, 1, v55
	v_mov_b32_e32 v63, v0
	v_ashrrev_i32_e32 v69, 31, v68
	v_lshl_add_u64 v[62:63], s[72:73], 0, v[62:63]
	v_lshlrev_b64 v[68:69], 11, v[68:69]
	v_lshl_add_u64 v[68:69], v[62:63], 0, v[68:69]
	global_store_dwordx4 v[68:69], v[64:67], off
	ds_read2_b32 v[64:65], v77 offset0:8 offset1:41
	s_waitcnt lgkmcnt(0)
	v_cvt_pk_bf16_f32 v64, v64, v65
	ds_read2_b32 v[66:67], v77 offset0:74 offset1:107
	s_waitcnt lgkmcnt(0)
	v_cvt_pk_bf16_f32 v65, v66, v67
	ds_read2_b32 v[66:67], v77 offset0:140 offset1:173
	s_waitcnt lgkmcnt(0)
	v_cvt_pk_bf16_f32 v66, v66, v67
	ds_read2_b32 v[68:69], v77 offset0:206 offset1:239
	s_waitcnt lgkmcnt(0)
	v_cvt_pk_bf16_f32 v67, v68, v69
	v_add_u32_e32 v68, s0, v79
	v_ashrrev_i32_e32 v69, 31, v68
	v_lshlrev_b64 v[68:69], 11, v[68:69]
	v_lshl_add_u64 v[68:69], v[62:63], 0, v[68:69]
	global_store_dwordx4 v[68:69], v[64:67], off
	ds_read2_b32 v[64:65], v77 offset0:16 offset1:49
	s_waitcnt lgkmcnt(0)
	v_cvt_pk_bf16_f32 v64, v64, v65
	ds_read2_b32 v[66:67], v77 offset0:82 offset1:115
	s_waitcnt lgkmcnt(0)
	v_cvt_pk_bf16_f32 v65, v66, v67
	ds_read2_b32 v[66:67], v77 offset0:148 offset1:181
	s_waitcnt lgkmcnt(0)
	v_cvt_pk_bf16_f32 v66, v66, v67
	ds_read2_b32 v[68:69], v77 offset0:214 offset1:247
	s_waitcnt lgkmcnt(0)
	v_cvt_pk_bf16_f32 v67, v68, v69
	v_add_u32_e32 v68, s0, v80
	v_ashrrev_i32_e32 v69, 31, v68
	v_lshlrev_b64 v[68:69], 11, v[68:69]
	v_lshl_add_u64 v[68:69], v[62:63], 0, v[68:69]
	global_store_dwordx4 v[68:69], v[64:67], off
	ds_read2_b32 v[64:65], v77 offset0:24 offset1:57
	s_waitcnt lgkmcnt(0)
	v_cvt_pk_bf16_f32 v64, v64, v65
	ds_read2_b32 v[66:67], v77 offset0:90 offset1:123
	s_waitcnt lgkmcnt(0)
	v_cvt_pk_bf16_f32 v65, v66, v67
	ds_read2_b32 v[66:67], v77 offset0:156 offset1:189
	s_waitcnt lgkmcnt(0)
	v_cvt_pk_bf16_f32 v66, v66, v67
	ds_read2_b32 v[68:69], v77 offset0:222 offset1:255
	s_waitcnt lgkmcnt(0)
	v_cvt_pk_bf16_f32 v67, v68, v69
	v_add_u32_e32 v68, s0, v81
	v_ashrrev_i32_e32 v69, 31, v68
	v_lshlrev_b64 v[68:69], 11, v[68:69]
	v_lshl_add_u64 v[62:63], v[62:63], 0, v[68:69]
	global_store_dwordx4 v[62:63], v[64:67], off
	s_waitcnt lgkmcnt(0)

;     ...
; #pragma unroll 8
;     for (int i = 0; i < 32; ++i) { const int kk = 2 * i + (lane >> 5); scr[kk * 33 + (lane & 31)] = W[(size_t)(k0 + kk) * ldw + n0 + (lane & 31)]; }
.LBB0_1249:
	s_lshl_b32 s36, s30, 1
	s_lshl_b32 s37, s1, 1
	v_add_u32_e32 v86, s36, v64
	v_add_u32_e32 v84, s37, v55
	v_ashrrev_i32_e32 v87, 31, v86
	v_ashrrev_i32_e32 v85, 31, v84
	v_lshlrev_b64 v[86:87], 12, v[86:87]
	v_lshlrev_b64 v[84:85], 12, v[84:85]
	v_lshl_add_u64 v[86:87], v[62:63], 0, v[86:87]
	v_lshl_add_u64 v[84:85], v[62:63], 0, v[84:85]
	global_load_dword v100, v[86:87], off
	global_load_dword v101, v[84:85], off
	v_add_u32_e32 v88, s37, v1
	v_add_u32_e32 v89, s36, v26
	v_mad_u64_u32 v[116:117], s[38:39], v89, s26, v[28:29]
	v_mad_u64_u32 v[118:119], s[38:39], v88, s26, v[28:29]
	v_add_u32_e32 v88, s37, v3
	v_add_u32_e32 v89, s36, v48
	s_add_i32 s30, s30, 16
	s_add_i32 s1, s1, 16
	s_add_i32 s5, s5, -16
	s_cmp_lg_u32 s5, 0
	v_add_u32_e32 v86, s36, v66
	v_add_u32_e32 v84, s37, v57
	v_ashrrev_i32_e32 v87, 31, v86
	v_ashrrev_i32_e32 v85, 31, v84
	v_lshlrev_b64 v[86:87], 12, v[86:87]
	v_lshlrev_b64 v[84:85], 12, v[84:85]
	v_lshl_add_u64 v[86:87], v[62:63], 0, v[86:87]
	v_lshl_add_u64 v[84:85], v[62:63], 0, v[84:85]
	global_load_dword v102, v[86:87], off
	global_load_dword v103, v[84:85], off
	v_mad_u64_u32 v[120:121], s[38:39], v89, s26, v[28:29]
	v_mad_u64_u32 v[122:123], s[38:39], v88, s26, v[28:29]
	v_add_u32_e32 v88, s37, v27
	v_add_u32_e32 v89, s36, v50
	v_add_u32_e32 v86, s36, v68
	v_add_u32_e32 v84, s37, v59
	v_ashrrev_i32_e32 v87, 31, v86
	v_ashrrev_i32_e32 v85, 31, v84
	v_lshlrev_b64 v[86:87], 12, v[86:87]
	v_lshlrev_b64 v[84:85], 12, v[84:85]
	v_lshl_add_u64 v[86:87], v[62:63], 0, v[86:87]
	v_lshl_add_u64 v[84:85], v[62:63], 0, v[84:85]
	global_load_dword v104, v[86:87], off
	global_load_dword v105, v[84:85], off
	v_mad_u64_u32 v[124:125], s[38:39], v89, s26, v[28:29]
	v_mad_u64_u32 v[126:127], s[38:39], v88, s26, v[28:29]
	v_add_u32_e32 v88, s37, v29
	v_add_u32_e32 v89, s36, v52
	v_add_u32_e32 v86, s36, v70
	v_add_u32_e32 v84, s37, v61
	v_ashrrev_i32_e32 v87, 31, v86
	v_ashrrev_i32_e32 v85, 31, v84
	v_lshlrev_b64 v[86:87], 12, v[86:87]
	v_lshlrev_b64 v[84:85], 12, v[84:85]
	v_lshl_add_u64 v[86:87], v[62:63], 0, v[86:87]
	v_lshl_add_u64 v[84:85], v[62:63], 0, v[84:85]
	global_load_dword v106, v[86:87], off
	global_load_dword v107, v[84:85], off
	v_mad_u64_u32 v[128:129], s[38:39], v89, s26, v[28:29]
	v_mad_u64_u32 v[130:131], s[38:39], v88, s26, v[28:29]
	v_add_u32_e32 v88, s37, v31
	v_add_u32_e32 v89, s36, v54
	v_add_u32_e32 v86, s36, v72
	v_add_u32_e32 v84, s37, v65
	v_ashrrev_i32_e32 v87, 31, v86
	v_ashrrev_i32_e32 v85, 31, v84
	v_lshlrev_b64 v[86:87], 12, v[86:87]
	v_lshlrev_b64 v[84:85], 12, v[84:85]
	v_lshl_add_u64 v[86:87], v[62:63], 0, v[86:87]
	v_lshl_add_u64 v[84:85], v[62:63], 0, v[84:85]
	global_load_dword v108, v[86:87], off
	global_load_dword v109, v[84:85], off
	v_mad_u64_u32 v[132:133], s[38:39], v89, s26, v[28:29]
	v_mad_u64_u32 v[134:135], s[38:39], v88, s26, v[28:29]
	v_add_u32_e32 v88, s37, v49
	v_add_u32_e32 v89, s36, v56
	v_add_u32_e32 v86, s36, v74
	v_add_u32_e32 v84, s37, v67
	v_ashrrev_i32_e32 v87, 31, v86
	v_ashrrev_i32_e32 v85, 31, v84
	v_lshlrev_b64 v[86:87], 12, v[86:87]
	v_lshlrev_b64 v[84:85], 12, v[84:85]
	v_lshl_add_u64 v[86:87], v[62:63], 0, v[86:87]
	v_lshl_add_u64 v[84:85], v[62:63], 0, v[84:85]
	global_load_dword v110, v[86:87], off
	global_load_dword v111, v[84:85], off
	v_mad_u64_u32 v[136:137], s[38:39], v89, s26, v[28:29]
	v_mad_u64_u32 v[138:139], s[38:39], v88, s26, v[28:29]
	v_add_u32_e32 v88, s37, v51
	v_add_u32_e32 v89, s36, v58
	v_add_u32_e32 v86, s36, v76
	v_add_u32_e32 v84, s37, v69
	v_ashrrev_i32_e32 v87, 31, v86
	v_ashrrev_i32_e32 v85, 31, v84
	v_lshlrev_b64 v[86:87], 12, v[86:87]
	v_lshlrev_b64 v[84:85], 12, v[84:85]
	v_lshl_add_u64 v[86:87], v[62:63], 0, v[86:87]
	v_lshl_add_u64 v[84:85], v[62:63], 0, v[84:85]
	global_load_dword v112, v[86:87], off
	global_load_dword v113, v[84:85], off
	v_mad_u64_u32 v[140:141], s[38:39], v89, s26, v[28:29]
	v_mad_u64_u32 v[142:143], s[38:39], v88, s26, v[28:29]
	v_add_u32_e32 v89, s36, v60
	v_add_u32_e32 v88, s37, v53
	v_add_u32_e32 v86, s36, v78
	v_add_u32_e32 v84, s37, v71
	v_ashrrev_i32_e32 v87, 31, v86
	v_ashrrev_i32_e32 v85, 31, v84
	v_lshlrev_b64 v[86:87], 12, v[86:87]
	v_lshlrev_b64 v[84:85], 12, v[84:85]
	v_lshl_add_u64 v[86:87], v[62:63], 0, v[86:87]
	v_lshl_add_u64 v[84:85], v[62:63], 0, v[84:85]
	global_load_dword v114, v[86:87], off
	global_load_dword v115, v[84:85], off
	v_mad_u64_u32 v[144:145], s[36:37], v89, s26, v[28:29]
	v_mad_u64_u32 v[146:147], s[36:37], v88, s26, v[28:29]
	s_waitcnt vmcnt(14)
	ds_write_b32 v116, v100
	ds_write_b32 v118, v101
	s_waitcnt vmcnt(12)
	ds_write_b32 v120, v102
	ds_write_b32 v122, v103
	s_waitcnt vmcnt(10)
	ds_write_b32 v124, v104
	ds_write_b32 v126, v105
	s_waitcnt vmcnt(8)
	ds_write_b32 v128, v106
	ds_write_b32 v130, v107
	s_waitcnt vmcnt(6)
	ds_write_b32 v132, v108
	ds_write_b32 v134, v109
	s_waitcnt vmcnt(4)
	ds_write_b32 v136, v110
	ds_write_b32 v138, v111
	s_waitcnt vmcnt(2)
	ds_write_b32 v140, v112
	ds_write_b32 v142, v113
	s_waitcnt vmcnt(0)
	ds_write_b32 v144, v114
	ds_write_b32 v146, v115
	s_cbranch_scc1 .LBB0_1249
; __device__ __forceinline__ unsigned cvt_pk_bf16(float lo, float hi) { unsigned r; asm volatile("v_cvt_pk_bf16_f32 %0, %1, %2" : "=v"(r) : "v"(lo), "v"(hi)); return r; }
; #define LAS __attribute__((address_space(3)))
;     ...
;     asm volatile("s_waitcnt lgkmcnt(0)" ::: "memory");
;     const int c = lane & 7;
; #pragma unroll
;     for (int j = 0; j < 4; ++j) { const int n = (lane >> 3) + 8 * j; const LAS float* s = scr + (8 * c) * 33 + n;
;         v4u o; o.x = cvt_pk_bf16(s[0 * 33], s[1 * 33]); o.y = cvt_pk_bf16(s[2 * 33], s[3 * 33]); o.z = cvt_pk_bf16(s[4 * 33], s[5 * 33]); o.w = cvt_pk_bf16(s[6 * 33], s[7 * 33]);
;         *(v4u*)(WT + (size_t)(row_off + n0 + n) * ldt + ((koff + k0 + 8 * c) ^ kx)) = o; }
;     asm volatile("s_waitcnt lgkmcnt(0)" ::: "memory");
	s_waitcnt lgkmcnt(0)
	ds_read2_b32 v[64:65], v77 offset1:33
	s_waitcnt lgkmcnt(0)
	v_cvt_pk_bf16_f32 v64, v64, v65
	ds_read2_b32 v[66:67], v77 offset0:66 offset1:99
	s_waitcnt lgkmcnt(0)
	v_cvt_pk_bf16_f32 v65, v66, v67
	ds_read2_b32 v[66:67], v77 offset0:132 offset1:165
	s_waitcnt lgkmcnt(0)
	v_cvt_pk_bf16_f32 v66, v66, v67
	ds_read2_b32 v[68:69], v77 offset0:198 offset1:231
	v_or_b32_e32 v55, s23, v75
	s_waitcnt lgkmcnt(0)
	v_cvt_pk_bf16_f32 v67, v68, v69
	v_add_u32_e32 v68, s0, v30
	v_lshlrev_b32_e32 v62, 1, v55
	v_mov_b32_e32 v63, v0
	v_ashrrev_i32_e32 v69, 31, v68
	v_lshl_add_u64 v[62:63], s[50:51], 0, v[62:63]
	v_lshlrev_b64 v[68:69], 8, v[68:69]
	v_lshl_add_u64 v[68:69], v[62:63], 0, v[68:69]
	global_store_dwordx4 v[68:69], v[64:67], off
	ds_read2_b32 v[64:65], v77 offset0:8 offset1:41
	s_waitcnt lgkmcnt(0)
	v_cvt_pk_bf16_f32 v64, v64, v65
	ds_read2_b32 v[66:67], v77 offset0:74 offset1:107
	s_waitcnt lgkmcnt(0)
	v_cvt_pk_bf16_f32 v65, v66, v67
	ds_read2_b32 v[66:67], v77 offset0:140 offset1:173
	s_waitcnt lgkmcnt(0)
	v_cvt_pk_bf16_f32 v66, v66, v67
	ds_read2_b32 v[68:69], v77 offset0:206 offset1:239
	s_waitcnt lgkmcnt(0)
	v_cvt_pk_bf16_f32 v67, v68, v69
	v_add_u32_e32 v68, s0, v79
	v_ashrrev_i32_e32 v69, 31, v68
	v_lshlrev_b64 v[68:69], 8, v[68:69]
	v_lshl_add_u64 v[68:69], v[62:63], 0, v[68:69]
	global_store_dwordx4 v[68:69], v[64:67], off
	ds_read2_b32 v[64:65], v77 offset0:16 offset1:49
	s_waitcnt lgkmcnt(0)
	v_cvt_pk_bf16_f32 v64, v64, v65
	ds_read2_b32 v[66:67], v77 offset0:82 offset1:115
	s_waitcnt lgkmcnt(0)
	v_cvt_pk_bf16_f32 v65, v66, v67
	ds_read2_b32 v[66:67], v77 offset0:148 offset1:181
	s_waitcnt lgkmcnt(0)
	v_cvt_pk_bf16_f32 v66, v66, v67
	ds_read2_b32 v[68:69], v77 offset0:214 offset1:247
	s_waitcnt lgkmcnt(0)
	v_cvt_pk_bf16_f32 v67, v68, v69
	v_add_u32_e32 v68, s0, v80
	v_ashrrev_i32_e32 v69, 31, v68
	v_lshlrev_b64 v[68:69], 8, v[68:69]
	v_lshl_add_u64 v[68:69], v[62:63], 0, v[68:69]
	global_store_dwordx4 v[68:69], v[64:67], off
	ds_read2_b32 v[64:65], v77 offset0:24 offset1:57
	s_waitcnt lgkmcnt(0)
	v_cvt_pk_bf16_f32 v64, v64, v65
	ds_read2_b32 v[66:67], v77 offset0:90 offset1:123
	s_waitcnt lgkmcnt(0)
	v_cvt_pk_bf16_f32 v65, v66, v67
	ds_read2_b32 v[66:67], v77 offset0:156 offset1:189
	s_waitcnt lgkmcnt(0)
	v_cvt_pk_bf16_f32 v66, v66, v67
	ds_read2_b32 v[68:69], v77 offset0:222 offset1:255
	s_waitcnt lgkmcnt(0)
	v_cvt_pk_bf16_f32 v67, v68, v69
	v_add_u32_e32 v68, s0, v81
	v_ashrrev_i32_e32 v69, 31, v68
	v_lshlrev_b64 v[68:69], 8, v[68:69]
	v_lshl_add_u64 v[62:63], v[62:63], 0, v[68:69]
	global_store_dwordx4 v[62:63], v[64:67], off
	s_waitcnt lgkmcnt(0)

;     ...
; #pragma unroll 8
;     for (int i = 0; i < 32; ++i) { const int kk = 2 * i + (lane >> 5); scr[kk * 33 + (lane & 31)] = W[(size_t)(k0 + kk) * ldw + n0 + (lane & 31)]; }
.LBB0_1254:
	s_lshl_b32 s23, s1, 1
	s_lshl_b32 s36, s0, 1
	v_add_u32_e32 v66, s23, v26
	v_add_u32_e32 v64, s36, v1
	v_ashrrev_i32_e32 v67, 31, v66
	v_ashrrev_i32_e32 v65, 31, v64
	v_lshlrev_b64 v[70:71], 12, v[66:67]
	v_lshlrev_b64 v[68:69], 12, v[64:65]
	v_lshl_add_u64 v[70:71], v[62:63], 0, v[70:71]
	v_lshl_add_u64 v[68:69], v[62:63], 0, v[68:69]
	global_load_dword v100, v[70:71], off offset:-4096
	global_load_dword v101, v[68:69], off offset:-4096
	v_mad_u64_u32 v[116:117], s[38:39], v66, s26, v[28:29]
	v_mad_u64_u32 v[118:119], s[38:39], v64, s26, v[28:29]
	s_add_i32 s1, s1, 16
	s_add_i32 s0, s0, 16
	s_add_i32 s5, s5, -16
	s_cmp_lg_u32 s5, 0
	v_add_u32_e32 v66, s23, v48
	v_add_u32_e32 v64, s36, v3
	v_ashrrev_i32_e32 v67, 31, v66
	v_ashrrev_i32_e32 v65, 31, v64
	v_lshlrev_b64 v[70:71], 12, v[66:67]
	v_lshlrev_b64 v[68:69], 12, v[64:65]
	v_lshl_add_u64 v[70:71], v[62:63], 0, v[70:71]
	v_lshl_add_u64 v[68:69], v[62:63], 0, v[68:69]
	global_load_dword v102, v[70:71], off offset:-4096
	global_load_dword v103, v[68:69], off offset:-4096
	v_mad_u64_u32 v[120:121], s[38:39], v66, s26, v[28:29]
	v_mad_u64_u32 v[122:123], s[38:39], v64, s26, v[28:29]
	v_add_u32_e32 v66, s23, v50
	v_add_u32_e32 v64, s36, v27
	v_ashrrev_i32_e32 v67, 31, v66
	v_ashrrev_i32_e32 v65, 31, v64
	v_lshlrev_b64 v[70:71], 12, v[66:67]
	v_lshlrev_b64 v[68:69], 12, v[64:65]
	v_lshl_add_u64 v[70:71], v[62:63], 0, v[70:71]
	v_lshl_add_u64 v[68:69], v[62:63], 0, v[68:69]
	global_load_dword v104, v[70:71], off offset:-4096
	global_load_dword v105, v[68:69], off offset:-4096
	v_mad_u64_u32 v[124:125], s[38:39], v66, s26, v[28:29]
	v_mad_u64_u32 v[126:127], s[38:39], v64, s26, v[28:29]
	v_add_u32_e32 v66, s23, v52
	v_add_u32_e32 v64, s36, v29
	v_ashrrev_i32_e32 v67, 31, v66
	v_ashrrev_i32_e32 v65, 31, v64
	v_lshlrev_b64 v[70:71], 12, v[66:67]
	v_lshlrev_b64 v[68:69], 12, v[64:65]
	v_lshl_add_u64 v[70:71], v[62:63], 0, v[70:71]
	v_lshl_add_u64 v[68:69], v[62:63], 0, v[68:69]
	global_load_dword v106, v[70:71], off offset:-4096
	global_load_dword v107, v[68:69], off offset:-4096
	v_mad_u64_u32 v[128:129], s[38:39], v66, s26, v[28:29]
	v_mad_u64_u32 v[130:131], s[38:39], v64, s26, v[28:29]
	v_add_u32_e32 v66, s23, v54
	v_add_u32_e32 v64, s36, v31
	v_ashrrev_i32_e32 v67, 31, v66
	v_ashrrev_i32_e32 v65, 31, v64
	v_lshlrev_b64 v[70:71], 12, v[66:67]
	v_lshlrev_b64 v[68:69], 12, v[64:65]
	v_lshl_add_u64 v[70:71], v[62:63], 0, v[70:71]
	v_lshl_add_u64 v[68:69], v[62:63], 0, v[68:69]
	global_load_dword v108, v[70:71], off offset:-4096
	global_load_dword v109, v[68:69], off offset:-4096
	v_mad_u64_u32 v[132:133], s[38:39], v66, s26, v[28:29]
	v_mad_u64_u32 v[134:135], s[38:39], v64, s26, v[28:29]
	v_add_u32_e32 v66, s23, v56
	v_add_u32_e32 v64, s36, v49
	v_ashrrev_i32_e32 v67, 31, v66
	v_ashrrev_i32_e32 v65, 31, v64
	v_lshlrev_b64 v[70:71], 12, v[66:67]
	v_lshlrev_b64 v[68:69], 12, v[64:65]
	v_lshl_add_u64 v[70:71], v[62:63], 0, v[70:71]
	v_lshl_add_u64 v[68:69], v[62:63], 0, v[68:69]
	global_load_dword v110, v[70:71], off offset:-4096
	global_load_dword v111, v[68:69], off offset:-4096
	v_mad_u64_u32 v[136:137], s[38:39], v66, s26, v[28:29]
	v_mad_u64_u32 v[138:139], s[38:39], v64, s26, v[28:29]
	v_add_u32_e32 v66, s23, v58
	v_add_u32_e32 v64, s36, v51
	v_ashrrev_i32_e32 v67, 31, v66
	v_ashrrev_i32_e32 v65, 31, v64
	v_lshlrev_b64 v[70:71], 12, v[66:67]
	v_lshlrev_b64 v[68:69], 12, v[64:65]
	v_lshl_add_u64 v[70:71], v[62:63], 0, v[70:71]
	v_lshl_add_u64 v[68:69], v[62:63], 0, v[68:69]
	global_load_dword v112, v[70:71], off offset:-4096
	global_load_dword v113, v[68:69], off offset:-4096
	v_mad_u64_u32 v[140:141], s[38:39], v66, s26, v[28:29]
	v_mad_u64_u32 v[142:143], s[38:39], v64, s26, v[28:29]
	v_add_u32_e32 v66, s23, v60
	v_add_u32_e32 v64, s36, v53
	v_ashrrev_i32_e32 v67, 31, v66
	v_ashrrev_i32_e32 v65, 31, v64
	v_lshlrev_b64 v[70:71], 12, v[66:67]
	v_lshlrev_b64 v[68:69], 12, v[64:65]
	v_lshl_add_u64 v[70:71], v[62:63], 0, v[70:71]
	v_lshl_add_u64 v[68:69], v[62:63], 0, v[68:69]
	global_load_dword v114, v[70:71], off offset:-4096
	global_load_dword v115, v[68:69], off offset:-4096
	v_mad_u64_u32 v[144:145], s[36:37], v66, s26, v[28:29]
	v_mad_u64_u32 v[146:147], s[36:37], v64, s26, v[28:29]
	s_waitcnt vmcnt(14)
	ds_write_b32 v116, v100
	ds_write_b32 v118, v101
	s_waitcnt vmcnt(12)
	ds_write_b32 v120, v102
	ds_write_b32 v122, v103
	s_waitcnt vmcnt(10)
	ds_write_b32 v124, v104
	ds_write_b32 v126, v105
	s_waitcnt vmcnt(8)
	ds_write_b32 v128, v106
	ds_write_b32 v130, v107
	s_waitcnt vmcnt(6)
	ds_write_b32 v132, v108
	ds_write_b32 v134, v109
	s_waitcnt vmcnt(4)
	ds_write_b32 v136, v110
	ds_write_b32 v138, v111
	s_waitcnt vmcnt(2)
	ds_write_b32 v140, v112
	ds_write_b32 v142, v113
	s_waitcnt vmcnt(0)
	ds_write_b32 v144, v114
	ds_write_b32 v146, v115
	s_cbranch_scc1 .LBB0_1254
; __device__ __forceinline__ unsigned cvt_pk_bf16(float lo, float hi) { unsigned r; asm volatile("v_cvt_pk_bf16_f32 %0, %1, %2" : "=v"(r) : "v"(lo), "v"(hi)); return r; }
; #define LAS __attribute__((address_space(3)))
;     ...
;     asm volatile("s_waitcnt lgkmcnt(0)" ::: "memory");
;     const int c = lane & 7;
; #pragma unroll
;     for (int j = 0; j < 4; ++j) { const int n = (lane >> 3) + 8 * j; const LAS float* s = scr + (8 * c) * 33 + n;
;         v4u o; o.x = cvt_pk_bf16(s[0 * 33], s[1 * 33]); o.y = cvt_pk_bf16(s[2 * 33], s[3 * 33]); o.z = cvt_pk_bf16(s[4 * 33], s[5 * 33]); o.w = cvt_pk_bf16(s[6 * 33], s[7 * 33]);
;         *(v4u*)(WT + (size_t)(row_off + n0 + n) * ldt + ((koff + k0 + 8 * c) ^ kx)) = o; }
;     asm volatile("s_waitcnt lgkmcnt(0)" ::: "memory");
	s_waitcnt lgkmcnt(0)
	ds_read2_b32 v[62:63], v77 offset1:33
	s_waitcnt lgkmcnt(0)
	v_cvt_pk_bf16_f32 v62, v62, v63
	ds_read2_b32 v[64:65], v77 offset0:66 offset1:99
	s_waitcnt lgkmcnt(0)
	v_cvt_pk_bf16_f32 v63, v64, v65
	ds_read2_b32 v[64:65], v77 offset0:132 offset1:165
	s_waitcnt lgkmcnt(0)
	v_cvt_pk_bf16_f32 v64, v64, v65
	ds_read2_b32 v[66:67], v77 offset0:198 offset1:231
	s_waitcnt lgkmcnt(0)
	v_cvt_pk_bf16_f32 v65, v66, v67
	v_add_u32_e32 v66, s30, v30
	v_ashrrev_i32_e32 v67, 31, v66
	v_lshlrev_b64 v[66:67], 8, v[66:67]
	v_lshl_add_u64 v[66:67], v[32:33], 0, v[66:67]
	global_store_dwordx4 v[66:67], v[62:65], off offset:128
	ds_read2_b32 v[62:63], v77 offset0:8 offset1:41
	s_waitcnt lgkmcnt(0)
	v_cvt_pk_bf16_f32 v62, v62, v63
	ds_read2_b32 v[64:65], v77 offset0:74 offset1:107
	s_waitcnt lgkmcnt(0)
	v_cvt_pk_bf16_f32 v63, v64, v65
	ds_read2_b32 v[64:65], v77 offset0:140 offset1:173
	s_waitcnt lgkmcnt(0)
	v_cvt_pk_bf16_f32 v64, v64, v65
	ds_read2_b32 v[66:67], v77 offset0:206 offset1:239
	s_waitcnt lgkmcnt(0)
	v_cvt_pk_bf16_f32 v65, v66, v67
	v_add_u32_e32 v66, s30, v79
	v_ashrrev_i32_e32 v67, 31, v66
	v_lshlrev_b64 v[66:67], 8, v[66:67]
	v_lshl_add_u64 v[66:67], v[32:33], 0, v[66:67]
	global_store_dwordx4 v[66:67], v[62:65], off offset:128
	ds_read2_b32 v[62:63], v77 offset0:16 offset1:49
	s_waitcnt lgkmcnt(0)
	v_cvt_pk_bf16_f32 v62, v62, v63
	ds_read2_b32 v[64:65], v77 offset0:82 offset1:115
	s_waitcnt lgkmcnt(0)
	v_cvt_pk_bf16_f32 v63, v64, v65
	ds_read2_b32 v[64:65], v77 offset0:148 offset1:181
	s_waitcnt lgkmcnt(0)
	v_cvt_pk_bf16_f32 v64, v64, v65
	ds_read2_b32 v[66:67], v77 offset0:214 offset1:247
	s_waitcnt lgkmcnt(0)
	v_cvt_pk_bf16_f32 v65, v66, v67
	v_add_u32_e32 v66, s30, v80
	v_ashrrev_i32_e32 v67, 31, v66
	v_lshlrev_b64 v[66:67], 8, v[66:67]
	v_lshl_add_u64 v[66:67], v[32:33], 0, v[66:67]
	global_store_dwordx4 v[66:67], v[62:65], off offset:128
	ds_read2_b32 v[62:63], v77 offset0:24 offset1:57
	s_waitcnt lgkmcnt(0)
	v_cvt_pk_bf16_f32 v62, v62, v63
	ds_read2_b32 v[64:65], v77 offset0:90 offset1:123
	s_waitcnt lgkmcnt(0)
	v_cvt_pk_bf16_f32 v63, v64, v65
	ds_read2_b32 v[64:65], v77 offset0:156 offset1:189
	s_waitcnt lgkmcnt(0)
	v_cvt_pk_bf16_f32 v64, v64, v65
	ds_read2_b32 v[66:67], v77 offset0:222 offset1:255
	s_waitcnt lgkmcnt(0)
	v_cvt_pk_bf16_f32 v65, v66, v67
	v_add_u32_e32 v66, s30, v81
	v_ashrrev_i32_e32 v67, 31, v66
	v_lshlrev_b64 v[66:67], 8, v[66:67]
	v_lshl_add_u64 v[66:67], v[32:33], 0, v[66:67]
	global_store_dwordx4 v[66:67], v[62:65], off offset:128
	s_waitcnt lgkmcnt(0)

;     ...
; #pragma unroll 8
;     for (int i = 0; i < 32; ++i) { const int kk = 2 * i + (lane >> 5); scr[kk * 33 + (lane & 31)] = W[(size_t)(k0 + kk) * ldw + n0 + (lane & 31)]; }
.LBB0_1259:
	s_lshl_b32 s22, s1, 1
	s_lshl_b32 s23, s0, 1
	v_add_u32_e32 v66, s22, v26
	v_add_u32_e32 v64, s23, v1
	v_ashrrev_i32_e32 v67, 31, v66
	v_ashrrev_i32_e32 v65, 31, v64
	v_lshlrev_b64 v[70:71], 12, v[66:67]
	v_lshlrev_b64 v[68:69], 12, v[64:65]
	v_lshl_add_u64 v[70:71], v[62:63], 0, v[70:71]
	v_lshl_add_u64 v[68:69], v[62:63], 0, v[68:69]
	global_load_dword v100, v[70:71], off
	global_load_dword v101, v[68:69], off
	v_mad_u64_u32 v[116:117], s[36:37], v66, s26, v[28:29]
	v_mad_u64_u32 v[118:119], s[36:37], v64, s26, v[28:29]
	s_add_i32 s1, s1, 16
	s_add_i32 s0, s0, 16
	s_add_i32 s5, s5, -16
	s_cmp_lg_u32 s5, 0
	v_add_u32_e32 v66, s22, v48
	v_add_u32_e32 v64, s23, v3
	v_ashrrev_i32_e32 v67, 31, v66
	v_ashrrev_i32_e32 v65, 31, v64
	v_lshlrev_b64 v[70:71], 12, v[66:67]
	v_lshlrev_b64 v[68:69], 12, v[64:65]
	v_lshl_add_u64 v[70:71], v[62:63], 0, v[70:71]
	v_lshl_add_u64 v[68:69], v[62:63], 0, v[68:69]
	global_load_dword v102, v[70:71], off
	global_load_dword v103, v[68:69], off
	v_mad_u64_u32 v[120:121], s[36:37], v66, s26, v[28:29]
	v_mad_u64_u32 v[122:123], s[36:37], v64, s26, v[28:29]
	v_add_u32_e32 v66, s22, v50
	v_add_u32_e32 v64, s23, v27
	v_ashrrev_i32_e32 v67, 31, v66
	v_ashrrev_i32_e32 v65, 31, v64
	v_lshlrev_b64 v[70:71], 12, v[66:67]
	v_lshlrev_b64 v[68:69], 12, v[64:65]
	v_lshl_add_u64 v[70:71], v[62:63], 0, v[70:71]
	v_lshl_add_u64 v[68:69], v[62:63], 0, v[68:69]
	global_load_dword v104, v[70:71], off
	global_load_dword v105, v[68:69], off
	v_mad_u64_u32 v[124:125], s[36:37], v66, s26, v[28:29]
	v_mad_u64_u32 v[126:127], s[36:37], v64, s26, v[28:29]
	v_add_u32_e32 v66, s22, v52
	v_add_u32_e32 v64, s23, v29
	v_ashrrev_i32_e32 v67, 31, v66
	v_ashrrev_i32_e32 v65, 31, v64
	v_lshlrev_b64 v[70:71], 12, v[66:67]
	v_lshlrev_b64 v[68:69], 12, v[64:65]
	v_lshl_add_u64 v[70:71], v[62:63], 0, v[70:71]
	v_lshl_add_u64 v[68:69], v[62:63], 0, v[68:69]
	global_load_dword v106, v[70:71], off
	global_load_dword v107, v[68:69], off
	v_mad_u64_u32 v[128:129], s[36:37], v66, s26, v[28:29]
	v_mad_u64_u32 v[130:131], s[36:37], v64, s26, v[28:29]
	v_add_u32_e32 v66, s22, v54
	v_add_u32_e32 v64, s23, v31
	v_ashrrev_i32_e32 v67, 31, v66
	v_ashrrev_i32_e32 v65, 31, v64
	v_lshlrev_b64 v[70:71], 12, v[66:67]
	v_lshlrev_b64 v[68:69], 12, v[64:65]
	v_lshl_add_u64 v[70:71], v[62:63], 0, v[70:71]
	v_lshl_add_u64 v[68:69], v[62:63], 0, v[68:69]
	global_load_dword v108, v[70:71], off
	global_load_dword v109, v[68:69], off
	v_mad_u64_u32 v[132:133], s[36:37], v66, s26, v[28:29]
	v_mad_u64_u32 v[134:135], s[36:37], v64, s26, v[28:29]
	v_add_u32_e32 v66, s22, v56
	v_add_u32_e32 v64, s23, v49
	v_ashrrev_i32_e32 v67, 31, v66
	v_ashrrev_i32_e32 v65, 31, v64
	v_lshlrev_b64 v[70:71], 12, v[66:67]
	v_lshlrev_b64 v[68:69], 12, v[64:65]
	v_lshl_add_u64 v[70:71], v[62:63], 0, v[70:71]
	v_lshl_add_u64 v[68:69], v[62:63], 0, v[68:69]
	global_load_dword v110, v[70:71], off
	global_load_dword v111, v[68:69], off
	v_mad_u64_u32 v[136:137], s[36:37], v66, s26, v[28:29]
	v_mad_u64_u32 v[138:139], s[36:37], v64, s26, v[28:29]
	v_add_u32_e32 v66, s22, v58
	v_add_u32_e32 v64, s23, v51
	v_ashrrev_i32_e32 v67, 31, v66
	v_ashrrev_i32_e32 v65, 31, v64
	v_lshlrev_b64 v[70:71], 12, v[66:67]
	v_lshlrev_b64 v[68:69], 12, v[64:65]
	v_lshl_add_u64 v[70:71], v[62:63], 0, v[70:71]
	v_lshl_add_u64 v[68:69], v[62:63], 0, v[68:69]
	global_load_dword v112, v[70:71], off
	global_load_dword v113, v[68:69], off
	v_mad_u64_u32 v[140:141], s[36:37], v66, s26, v[28:29]
	v_mad_u64_u32 v[142:143], s[36:37], v64, s26, v[28:29]
	v_add_u32_e32 v66, s22, v60
	v_add_u32_e32 v64, s23, v53
	v_ashrrev_i32_e32 v67, 31, v66
	v_ashrrev_i32_e32 v65, 31, v64
	v_lshlrev_b64 v[70:71], 12, v[66:67]
	v_lshlrev_b64 v[68:69], 12, v[64:65]
	v_lshl_add_u64 v[70:71], v[62:63], 0, v[70:71]
	v_lshl_add_u64 v[68:69], v[62:63], 0, v[68:69]
	global_load_dword v114, v[70:71], off
	global_load_dword v115, v[68:69], off
	v_mad_u64_u32 v[144:145], s[22:23], v66, s26, v[28:29]
	v_mad_u64_u32 v[146:147], s[22:23], v64, s26, v[28:29]
	s_waitcnt vmcnt(14)
	ds_write_b32 v116, v100
	ds_write_b32 v118, v101
	s_waitcnt vmcnt(12)
	ds_write_b32 v120, v102
	ds_write_b32 v122, v103
	s_waitcnt vmcnt(10)
	ds_write_b32 v124, v104
	ds_write_b32 v126, v105
	s_waitcnt vmcnt(8)
	ds_write_b32 v128, v106
	ds_write_b32 v130, v107
	s_waitcnt vmcnt(6)
	ds_write_b32 v132, v108
	ds_write_b32 v134, v109
	s_waitcnt vmcnt(4)
	ds_write_b32 v136, v110
	ds_write_b32 v138, v111
	s_waitcnt vmcnt(2)
	ds_write_b32 v140, v112
	ds_write_b32 v142, v113
	s_waitcnt vmcnt(0)
	ds_write_b32 v144, v114
	ds_write_b32 v146, v115
	s_cbranch_scc1 .LBB0_1259
; __device__ __forceinline__ unsigned cvt_pk_bf16(float lo, float hi) { unsigned r; asm volatile("v_cvt_pk_bf16_f32 %0, %1, %2" : "=v"(r) : "v"(lo), "v"(hi)); return r; }
; #define LAS __attribute__((address_space(3)))
;     ...
;     asm volatile("s_waitcnt lgkmcnt(0)" ::: "memory");
;     const int c = lane & 7;
; #pragma unroll
;     for (int j = 0; j < 4; ++j) { const int n = (lane >> 3) + 8 * j; const LAS float* s = scr + (8 * c) * 33 + n;
;         v4u o; o.x = cvt_pk_bf16(s[0 * 33], s[1 * 33]); o.y = cvt_pk_bf16(s[2 * 33], s[3 * 33]); o.z = cvt_pk_bf16(s[4 * 33], s[5 * 33]); o.w = cvt_pk_bf16(s[6 * 33], s[7 * 33]);
;         *(v4u*)(WT + (size_t)(row_off + n0 + n) * ldt + ((koff + k0 + 8 * c) ^ kx)) = o; }
;     asm volatile("s_waitcnt lgkmcnt(0)" ::: "memory");
	s_waitcnt lgkmcnt(0)
	ds_read2_b32 v[62:63], v77 offset1:33
	s_waitcnt lgkmcnt(0)
	v_cvt_pk_bf16_f32 v62, v62, v63
	ds_read2_b32 v[64:65], v77 offset0:66 offset1:99
	s_waitcnt lgkmcnt(0)
	v_cvt_pk_bf16_f32 v63, v64, v65
	ds_read2_b32 v[64:65], v77 offset0:132 offset1:165
	s_waitcnt lgkmcnt(0)
	v_cvt_pk_bf16_f32 v64, v64, v65
	ds_read2_b32 v[66:67], v77 offset0:198 offset1:231
	s_waitcnt lgkmcnt(0)
	v_cvt_pk_bf16_f32 v65, v66, v67
	v_add_u32_e32 v66, s30, v30
	v_ashrrev_i32_e32 v67, 31, v66
	v_lshlrev_b64 v[66:67], 8, v[66:67]
	v_lshl_add_u64 v[66:67], v[32:33], 0, v[66:67]
	global_store_dwordx4 v[66:67], v[62:65], off
	ds_read2_b32 v[62:63], v77 offset0:8 offset1:41
	s_waitcnt lgkmcnt(0)
	v_cvt_pk_bf16_f32 v62, v62, v63
	ds_read2_b32 v[64:65], v77 offset0:74 offset1:107
	s_waitcnt lgkmcnt(0)
	v_cvt_pk_bf16_f32 v63, v64, v65
	ds_read2_b32 v[64:65], v77 offset0:140 offset1:173
	s_waitcnt lgkmcnt(0)
	v_cvt_pk_bf16_f32 v64, v64, v65
	ds_read2_b32 v[66:67], v77 offset0:206 offset1:239
	s_waitcnt lgkmcnt(0)
	v_cvt_pk_bf16_f32 v65, v66, v67
	v_add_u32_e32 v66, s30, v79
	v_ashrrev_i32_e32 v67, 31, v66
	v_lshlrev_b64 v[66:67], 8, v[66:67]
	v_lshl_add_u64 v[66:67], v[32:33], 0, v[66:67]
	global_store_dwordx4 v[66:67], v[62:65], off
	ds_read2_b32 v[62:63], v77 offset0:16 offset1:49
	s_waitcnt lgkmcnt(0)
	v_cvt_pk_bf16_f32 v62, v62, v63
	ds_read2_b32 v[64:65], v77 offset0:82 offset1:115
	s_waitcnt lgkmcnt(0)
	v_cvt_pk_bf16_f32 v63, v64, v65
	ds_read2_b32 v[64:65], v77 offset0:148 offset1:181
	s_waitcnt lgkmcnt(0)
	v_cvt_pk_bf16_f32 v64, v64, v65
	ds_read2_b32 v[66:67], v77 offset0:214 offset1:247
	s_waitcnt lgkmcnt(0)
	v_cvt_pk_bf16_f32 v65, v66, v67
	v_add_u32_e32 v66, s30, v80
	v_ashrrev_i32_e32 v67, 31, v66
	v_lshlrev_b64 v[66:67], 8, v[66:67]
	v_lshl_add_u64 v[66:67], v[32:33], 0, v[66:67]
	global_store_dwordx4 v[66:67], v[62:65], off
	ds_read2_b32 v[62:63], v77 offset0:24 offset1:57
	s_waitcnt lgkmcnt(0)
	v_cvt_pk_bf16_f32 v62, v62, v63
	ds_read2_b32 v[64:65], v77 offset0:90 offset1:123
	s_waitcnt lgkmcnt(0)
	v_cvt_pk_bf16_f32 v63, v64, v65
	ds_read2_b32 v[64:65], v77 offset0:156 offset1:189
	s_waitcnt lgkmcnt(0)
	v_cvt_pk_bf16_f32 v64, v64, v65
	ds_read2_b32 v[66:67], v77 offset0:222 offset1:255
	s_waitcnt lgkmcnt(0)
	v_cvt_pk_bf16_f32 v65, v66, v67
	v_add_u32_e32 v66, s30, v81
	v_ashrrev_i32_e32 v67, 31, v66
	v_lshlrev_b64 v[66:67], 8, v[66:67]
	v_lshl_add_u64 v[66:67], v[32:33], 0, v[66:67]
	global_store_dwordx4 v[66:67], v[62:65], off
	s_waitcnt lgkmcnt(0)

;     ...
; #pragma unroll 8
;     for (int i = 0; i < 32; ++i) { const int kk = 2 * i + (lane >> 5); scr[kk * 33 + (lane & 31)] = W[(size_t)(k0 + kk) * ldw + n0 + (lane & 31)]; }
.LBB0_1264:
	s_lshl_b32 s22, s5, 1
	s_lshl_b32 s23, s1, 1
	v_add_u32_e32 v86, s22, v62
	v_add_u32_e32 v84, s23, v55
	v_ashrrev_i32_e32 v87, 31, v86
	v_ashrrev_i32_e32 v85, 31, v84
	v_lshlrev_b64 v[86:87], 7, v[86:87]
	v_lshlrev_b64 v[84:85], 7, v[84:85]
	v_lshl_add_u64 v[86:87], v[22:23], 0, v[86:87]
	v_lshl_add_u64 v[84:85], v[22:23], 0, v[84:85]
	global_load_dword v100, v[86:87], off
	global_load_dword v101, v[84:85], off
	v_add_u32_e32 v71, s23, v1
	v_add_u32_e32 v78, s22, v26
	v_mad_u64_u32 v[116:117], s[36:37], v78, s26, v[28:29]
	v_mad_u64_u32 v[118:119], s[36:37], v71, s26, v[28:29]
	v_add_u32_e32 v71, s23, v3
	v_add_u32_e32 v78, s22, v48
	s_add_i32 s5, s5, 16
	s_add_i32 s1, s1, 16
	s_add_i32 s21, s21, -16
	s_cmp_lg_u32 s21, 0
	v_add_u32_e32 v86, s22, v64
	v_add_u32_e32 v84, s23, v57
	v_ashrrev_i32_e32 v87, 31, v86
	v_ashrrev_i32_e32 v85, 31, v84
	v_lshlrev_b64 v[86:87], 7, v[86:87]
	v_lshlrev_b64 v[84:85], 7, v[84:85]
	v_lshl_add_u64 v[86:87], v[22:23], 0, v[86:87]
	v_lshl_add_u64 v[84:85], v[22:23], 0, v[84:85]
	global_load_dword v102, v[86:87], off
	global_load_dword v103, v[84:85], off
	v_mad_u64_u32 v[120:121], s[36:37], v78, s26, v[28:29]
	v_mad_u64_u32 v[122:123], s[36:37], v71, s26, v[28:29]
	v_add_u32_e32 v71, s23, v27
	v_add_u32_e32 v78, s22, v50
	v_add_u32_e32 v86, s22, v66
	v_add_u32_e32 v84, s23, v59
	v_ashrrev_i32_e32 v87, 31, v86
	v_ashrrev_i32_e32 v85, 31, v84
	v_lshlrev_b64 v[86:87], 7, v[86:87]
	v_lshlrev_b64 v[84:85], 7, v[84:85]
	v_lshl_add_u64 v[86:87], v[22:23], 0, v[86:87]
	v_lshl_add_u64 v[84:85], v[22:23], 0, v[84:85]
	global_load_dword v104, v[86:87], off
	global_load_dword v105, v[84:85], off
	v_mad_u64_u32 v[124:125], s[36:37], v78, s26, v[28:29]
	v_mad_u64_u32 v[126:127], s[36:37], v71, s26, v[28:29]
	v_add_u32_e32 v71, s23, v29
	v_add_u32_e32 v78, s22, v52
	v_add_u32_e32 v86, s22, v68
	v_add_u32_e32 v84, s23, v61
	v_ashrrev_i32_e32 v87, 31, v86
	v_ashrrev_i32_e32 v85, 31, v84
	v_lshlrev_b64 v[86:87], 7, v[86:87]
	v_lshlrev_b64 v[84:85], 7, v[84:85]
	v_lshl_add_u64 v[86:87], v[22:23], 0, v[86:87]
	v_lshl_add_u64 v[84:85], v[22:23], 0, v[84:85]
	global_load_dword v106, v[86:87], off
	global_load_dword v107, v[84:85], off
	v_mad_u64_u32 v[128:129], s[36:37], v78, s26, v[28:29]
	v_mad_u64_u32 v[130:131], s[36:37], v71, s26, v[28:29]
	v_add_u32_e32 v71, s23, v31
	v_add_u32_e32 v78, s22, v54
	v_add_u32_e32 v86, s22, v70
	v_add_u32_e32 v84, s23, v63
	v_ashrrev_i32_e32 v87, 31, v86
	v_ashrrev_i32_e32 v85, 31, v84
	v_lshlrev_b64 v[86:87], 7, v[86:87]
	v_lshlrev_b64 v[84:85], 7, v[84:85]
	v_lshl_add_u64 v[86:87], v[22:23], 0, v[86:87]
	v_lshl_add_u64 v[84:85], v[22:23], 0, v[84:85]
	global_load_dword v108, v[86:87], off
	global_load_dword v109, v[84:85], off
	v_mad_u64_u32 v[132:133], s[36:37], v78, s26, v[28:29]
	v_mad_u64_u32 v[134:135], s[36:37], v71, s26, v[28:29]
	v_add_u32_e32 v71, s23, v49
	v_add_u32_e32 v78, s22, v56
	v_add_u32_e32 v86, s22, v72
	v_add_u32_e32 v84, s23, v65
	v_ashrrev_i32_e32 v87, 31, v86
	v_ashrrev_i32_e32 v85, 31, v84
	v_lshlrev_b64 v[86:87], 7, v[86:87]
	v_lshlrev_b64 v[84:85], 7, v[84:85]
	v_lshl_add_u64 v[86:87], v[22:23], 0, v[86:87]
	v_lshl_add_u64 v[84:85], v[22:23], 0, v[84:85]
	global_load_dword v110, v[86:87], off
	global_load_dword v111, v[84:85], off
	v_mad_u64_u32 v[136:137], s[36:37], v78, s26, v[28:29]
	v_mad_u64_u32 v[138:139], s[36:37], v71, s26, v[28:29]
	v_add_u32_e32 v71, s23, v51
	v_add_u32_e32 v78, s22, v58
	v_add_u32_e32 v86, s22, v74
	v_add_u32_e32 v84, s23, v67
	v_ashrrev_i32_e32 v87, 31, v86
	v_ashrrev_i32_e32 v85, 31, v84
	v_lshlrev_b64 v[86:87], 7, v[86:87]
	v_lshlrev_b64 v[84:85], 7, v[84:85]
	v_lshl_add_u64 v[86:87], v[22:23], 0, v[86:87]
	v_lshl_add_u64 v[84:85], v[22:23], 0, v[84:85]
	global_load_dword v112, v[86:87], off
	global_load_dword v113, v[84:85], off
	v_mad_u64_u32 v[140:141], s[36:37], v78, s26, v[28:29]
	v_mad_u64_u32 v[142:143], s[36:37], v71, s26, v[28:29]
	v_add_u32_e32 v78, s22, v60
	v_add_u32_e32 v71, s23, v53
	v_add_u32_e32 v86, s22, v76
	v_add_u32_e32 v84, s23, v69
	v_ashrrev_i32_e32 v87, 31, v86
	v_ashrrev_i32_e32 v85, 31, v84
	v_lshlrev_b64 v[86:87], 7, v[86:87]
	v_lshlrev_b64 v[84:85], 7, v[84:85]
	v_lshl_add_u64 v[86:87], v[22:23], 0, v[86:87]
	v_lshl_add_u64 v[84:85], v[22:23], 0, v[84:85]
	global_load_dword v114, v[86:87], off
	global_load_dword v115, v[84:85], off
	v_mad_u64_u32 v[144:145], s[22:23], v78, s26, v[28:29]
	v_mad_u64_u32 v[146:147], s[22:23], v71, s26, v[28:29]
	s_waitcnt vmcnt(14)
	ds_write_b32 v116, v100
	ds_write_b32 v118, v101
	s_waitcnt vmcnt(12)
	ds_write_b32 v120, v102
	ds_write_b32 v122, v103
	s_waitcnt vmcnt(10)
	ds_write_b32 v124, v104
	ds_write_b32 v126, v105
	s_waitcnt vmcnt(8)
	ds_write_b32 v128, v106
	ds_write_b32 v130, v107
	s_waitcnt vmcnt(6)
	ds_write_b32 v132, v108
	ds_write_b32 v134, v109
	s_waitcnt vmcnt(4)
	ds_write_b32 v136, v110
	ds_write_b32 v138, v111
	s_waitcnt vmcnt(2)
	ds_write_b32 v140, v112
	ds_write_b32 v142, v113
	s_waitcnt vmcnt(0)
	ds_write_b32 v144, v114
	ds_write_b32 v146, v115
	s_cbranch_scc1 .LBB0_1264
; __device__ __forceinline__ unsigned cvt_pk_bf16(float lo, float hi) { unsigned r; asm volatile("v_cvt_pk_bf16_f32 %0, %1, %2" : "=v"(r) : "v"(lo), "v"(hi)); return r; }
; #define LAS __attribute__((address_space(3)))
;     ...
;     asm volatile("s_waitcnt lgkmcnt(0)" ::: "memory");
;     const int c = lane & 7;
; #pragma unroll
;     for (int j = 0; j < 4; ++j) { const int n = (lane >> 3) + 8 * j; const LAS float* s = scr + (8 * c) * 33 + n;
;         v4u o; o.x = cvt_pk_bf16(s[0 * 33], s[1 * 33]); o.y = cvt_pk_bf16(s[2 * 33], s[3 * 33]); o.z = cvt_pk_bf16(s[4 * 33], s[5 * 33]); o.w = cvt_pk_bf16(s[6 * 33], s[7 * 33]);
;         *(v4u*)(WT + (size_t)(row_off + n0 + n) * ldt + ((koff + k0 + 8 * c) ^ kx)) = o; }
;     asm volatile("s_waitcnt lgkmcnt(0)" ::: "memory");
	v_mov_b32_e32 v55, 0x400
	v_bitop3_b32 v55, s0, v55, v75 bitop3:0x36
	s_waitcnt lgkmcnt(0)
	v_lshlrev_b32_e32 v62, 1, v55
	v_mov_b32_e32 v63, v0
	v_lshl_add_u64 v[66:67], s[82:83], 0, v[62:63]
	ds_read2_b32 v[62:63], v77 offset1:33
	s_waitcnt lgkmcnt(0)
	v_cvt_pk_bf16_f32 v62, v62, v63
	ds_read2_b32 v[64:65], v77 offset0:66 offset1:99
	s_waitcnt lgkmcnt(0)
	v_cvt_pk_bf16_f32 v63, v64, v65
	ds_read2_b32 v[64:65], v77 offset0:132 offset1:165
	s_waitcnt lgkmcnt(0)
	v_cvt_pk_bf16_f32 v64, v64, v65
	ds_read2_b32 v[68:69], v77 offset0:198 offset1:231
	s_waitcnt lgkmcnt(0)
	v_cvt_pk_bf16_f32 v65, v68, v69
	v_lshl_add_u64 v[68:69], v[66:67], 0, v[34:35]
	global_store_dwordx4 v[68:69], v[62:65], off
	ds_read2_b32 v[62:63], v77 offset0:8 offset1:41
	s_waitcnt lgkmcnt(0)
	v_cvt_pk_bf16_f32 v62, v62, v63
	ds_read2_b32 v[64:65], v77 offset0:74 offset1:107
	s_waitcnt lgkmcnt(0)
	v_cvt_pk_bf16_f32 v63, v64, v65
	ds_read2_b32 v[64:65], v77 offset0:140 offset1:173
	s_waitcnt lgkmcnt(0)
	v_cvt_pk_bf16_f32 v64, v64, v65
	ds_read2_b32 v[68:69], v77 offset0:206 offset1:239
	s_waitcnt lgkmcnt(0)
	v_cvt_pk_bf16_f32 v65, v68, v69
	v_lshl_add_u64 v[68:69], v[66:67], 0, v[36:37]
	global_store_dwordx4 v[68:69], v[62:65], off
	ds_read2_b32 v[62:63], v77 offset0:16 offset1:49
	s_waitcnt lgkmcnt(0)
	v_cvt_pk_bf16_f32 v62, v62, v63
	ds_read2_b32 v[64:65], v77 offset0:82 offset1:115
	s_waitcnt lgkmcnt(0)
	v_cvt_pk_bf16_f32 v63, v64, v65
	ds_read2_b32 v[64:65], v77 offset0:148 offset1:181
	s_waitcnt lgkmcnt(0)
	v_cvt_pk_bf16_f32 v64, v64, v65
	ds_read2_b32 v[68:69], v77 offset0:214 offset1:247
	s_waitcnt lgkmcnt(0)
	v_cvt_pk_bf16_f32 v65, v68, v69
	v_lshl_add_u64 v[68:69], v[66:67], 0, v[38:39]
	global_store_dwordx4 v[68:69], v[62:65], off
	ds_read2_b32 v[62:63], v77 offset0:24 offset1:57
	v_lshl_add_u64 v[66:67], v[66:67], 0, v[40:41]
	s_waitcnt lgkmcnt(0)
	v_cvt_pk_bf16_f32 v62, v62, v63
	ds_read2_b32 v[64:65], v77 offset0:90 offset1:123
	s_waitcnt lgkmcnt(0)
	v_cvt_pk_bf16_f32 v63, v64, v65
	ds_read2_b32 v[64:65], v77 offset0:156 offset1:189
	s_waitcnt lgkmcnt(0)
	v_cvt_pk_bf16_f32 v64, v64, v65
	ds_read2_b32 v[68:69], v77 offset0:222 offset1:255
	s_waitcnt lgkmcnt(0)
	v_cvt_pk_bf16_f32 v65, v68, v69
	global_store_dwordx4 v[66:67], v[62:65], off
	s_waitcnt lgkmcnt(0)

; __device__ __forceinline__ unsigned cvt_pk_bf16(float lo, float hi) { unsigned r; asm volatile("v_cvt_pk_bf16_f32 %0, %1, %2" : "=v"(r) : "v"(lo), "v"(hi)); return r; }
; #define LAS __attribute__((address_space(3)))
;     ...
; #pragma unroll 8
;     for (int i = 0; i < 32; ++i) { const int kk = 2 * i + (lane >> 5); scr[kk * 33 + (lane & 31)] = W[(size_t)(k0 + kk) * ldw + n0 + (lane & 31)]; }
;     asm volatile("s_waitcnt lgkmcnt(0)" ::: "memory");
;     const int c = lane & 7;
; #pragma unroll
;     for (int j = 0; j < 4; ++j) { const int n = (lane >> 3) + 8 * j; const LAS float* s = scr + (8 * c) * 33 + n;
;         v4u o; o.x = cvt_pk_bf16(s[0 * 33], s[1 * 33]); o.y = cvt_pk_bf16(s[2 * 33], s[3 * 33]); o.z = cvt_pk_bf16(s[4 * 33], s[5 * 33]); o.w = cvt_pk_bf16(s[6 * 33], s[7 * 33]);
;         *(v4u*)(WT + (size_t)(row_off + n0 + n) * ldt + ((koff + k0 + 8 * c) ^ kx)) = o; }
;     asm volatile("s_waitcnt lgkmcnt(0)" ::: "memory");
.LBB0_1269:
	s_lshl_b32 s23, s21, 1
	s_lshl_b32 s30, s1, 1
	v_add_u32_e32 v84, s23, v64
	v_add_u32_e32 v86, s30, v55
	v_mad_i64_i32 v[84:85], s[36:37], v84, s80, v[62:63]
	v_mad_i64_i32 v[86:87], s[36:37], v86, s80, v[62:63]
	global_load_dword v100, v[84:85], off
	global_load_dword v101, v[86:87], off
	v_add_u32_e32 v89, s23, v26
	v_add_u32_e32 v88, s30, v1
	v_mad_u64_u32 v[116:117], s[36:37], v89, s26, v[28:29]
	v_mad_u64_u32 v[118:119], s[36:37], v88, s26, v[28:29]
	v_add_u32_e32 v89, s23, v48
	v_add_u32_e32 v88, s30, v3
	s_add_i32 s21, s21, 16
	s_add_i32 s1, s1, 16
	s_add_i32 s22, s22, -16
	s_cmp_lg_u32 s22, 0
	v_add_u32_e32 v84, s23, v66
	v_add_u32_e32 v86, s30, v57
	v_mad_i64_i32 v[84:85], s[36:37], v84, s80, v[62:63]
	v_mad_i64_i32 v[86:87], s[36:37], v86, s80, v[62:63]
	global_load_dword v102, v[84:85], off
	global_load_dword v103, v[86:87], off
	v_mad_u64_u32 v[120:121], s[36:37], v89, s26, v[28:29]
	v_mad_u64_u32 v[122:123], s[36:37], v88, s26, v[28:29]
	v_add_u32_e32 v89, s23, v50
	v_add_u32_e32 v88, s30, v27
	v_add_u32_e32 v84, s23, v68
	v_add_u32_e32 v86, s30, v59
	v_mad_i64_i32 v[84:85], s[36:37], v84, s80, v[62:63]
	v_mad_i64_i32 v[86:87], s[36:37], v86, s80, v[62:63]
	global_load_dword v104, v[84:85], off
	global_load_dword v105, v[86:87], off
	v_mad_u64_u32 v[124:125], s[36:37], v89, s26, v[28:29]
	v_mad_u64_u32 v[126:127], s[36:37], v88, s26, v[28:29]
	v_add_u32_e32 v89, s23, v52
	v_add_u32_e32 v88, s30, v29
	v_add_u32_e32 v84, s23, v70
	v_add_u32_e32 v86, s30, v61
	v_mad_i64_i32 v[84:85], s[36:37], v84, s80, v[62:63]
	v_mad_i64_i32 v[86:87], s[36:37], v86, s80, v[62:63]
	global_load_dword v106, v[84:85], off
	global_load_dword v107, v[86:87], off
	v_mad_u64_u32 v[128:129], s[36:37], v89, s26, v[28:29]
	v_mad_u64_u32 v[130:131], s[36:37], v88, s26, v[28:29]
	v_add_u32_e32 v89, s23, v54
	v_add_u32_e32 v88, s30, v31
	v_add_u32_e32 v84, s23, v72
	v_add_u32_e32 v86, s30, v65
	v_mad_i64_i32 v[84:85], s[36:37], v84, s80, v[62:63]
	v_mad_i64_i32 v[86:87], s[36:37], v86, s80, v[62:63]
	global_load_dword v108, v[84:85], off
	global_load_dword v109, v[86:87], off
	v_mad_u64_u32 v[132:133], s[36:37], v89, s26, v[28:29]
	v_mad_u64_u32 v[134:135], s[36:37], v88, s26, v[28:29]
	v_add_u32_e32 v89, s23, v56
	v_add_u32_e32 v88, s30, v49
	v_add_u32_e32 v84, s23, v74
	v_add_u32_e32 v86, s30, v67
	v_mad_i64_i32 v[84:85], s[36:37], v84, s80, v[62:63]
	v_mad_i64_i32 v[86:87], s[36:37], v86, s80, v[62:63]
	global_load_dword v110, v[84:85], off
	global_load_dword v111, v[86:87], off
	v_mad_u64_u32 v[136:137], s[36:37], v89, s26, v[28:29]
	v_mad_u64_u32 v[138:139], s[36:37], v88, s26, v[28:29]
	v_add_u32_e32 v89, s23, v58
	v_add_u32_e32 v88, s30, v51
	v_add_u32_e32 v84, s23, v76
	v_add_u32_e32 v86, s30, v69
	v_mad_i64_i32 v[84:85], s[36:37], v84, s80, v[62:63]
	v_mad_i64_i32 v[86:87], s[36:37], v86, s80, v[62:63]
	global_load_dword v112, v[84:85], off
	global_load_dword v113, v[86:87], off
	v_mad_u64_u32 v[140:141], s[36:37], v89, s26, v[28:29]
	v_mad_u64_u32 v[142:143], s[36:37], v88, s26, v[28:29]
	v_add_u32_e32 v89, s23, v60
	v_add_u32_e32 v88, s30, v53
	v_add_u32_e32 v84, s23, v78
	v_add_u32_e32 v86, s30, v71
	v_mad_i64_i32 v[84:85], s[36:37], v84, s80, v[62:63]
	v_mad_i64_i32 v[86:87], s[36:37], v86, s80, v[62:63]
	global_load_dword v114, v[84:85], off
	global_load_dword v115, v[86:87], off
	v_mad_u64_u32 v[144:145], s[36:37], v89, s26, v[28:29]
	v_mad_u64_u32 v[146:147], s[36:37], v88, s26, v[28:29]
	s_waitcnt vmcnt(14)
	ds_write_b32 v116, v100
	ds_write_b32 v118, v101
	s_waitcnt vmcnt(12)
	ds_write_b32 v120, v102
	ds_write_b32 v122, v103
	s_waitcnt vmcnt(10)
	ds_write_b32 v124, v104
	ds_write_b32 v126, v105
	s_waitcnt vmcnt(8)
	ds_write_b32 v128, v106
	ds_write_b32 v130, v107
	s_waitcnt vmcnt(6)
	ds_write_b32 v132, v108
	ds_write_b32 v134, v109
	s_waitcnt vmcnt(4)
	ds_write_b32 v136, v110
	ds_write_b32 v138, v111
	s_waitcnt vmcnt(2)
	ds_write_b32 v140, v112
	ds_write_b32 v142, v113
	s_waitcnt vmcnt(0)
	ds_write_b32 v144, v114
	ds_write_b32 v146, v115
	s_cbranch_scc1 .LBB0_1269
	s_waitcnt lgkmcnt(0)
	ds_read2_b32 v[64:65], v77 offset1:33
	s_waitcnt lgkmcnt(0)
	v_cvt_pk_bf16_f32 v64, v64, v65
	ds_read2_b32 v[66:67], v77 offset0:66 offset1:99
	s_waitcnt lgkmcnt(0)
	v_cvt_pk_bf16_f32 v65, v66, v67
	ds_read2_b32 v[66:67], v77 offset0:132 offset1:165
	v_mov_b32_e32 v55, 0x400
	s_waitcnt lgkmcnt(0)
	v_cvt_pk_bf16_f32 v66, v66, v67
	ds_read2_b32 v[68:69], v77 offset0:198 offset1:231
	v_bitop3_b32 v55, s5, v55, v75 bitop3:0x36
	s_waitcnt lgkmcnt(0)
	v_cvt_pk_bf16_f32 v67, v68, v69
	v_add_u32_e32 v68, s0, v30
	v_lshlrev_b32_e32 v62, 1, v55
	v_mov_b32_e32 v63, v0
	v_ashrrev_i32_e32 v69, 31, v68
	v_lshl_add_u64 v[62:63], s[54:55], 0, v[62:63]
	v_lshlrev_b64 v[68:69], 12, v[68:69]
	v_lshl_add_u64 v[68:69], v[62:63], 0, v[68:69]
	global_store_dwordx4 v[68:69], v[64:67], off
	ds_read2_b32 v[64:65], v77 offset0:8 offset1:41
	s_waitcnt lgkmcnt(0)
	v_cvt_pk_bf16_f32 v64, v64, v65
	ds_read2_b32 v[66:67], v77 offset0:74 offset1:107
	s_waitcnt lgkmcnt(0)
	v_cvt_pk_bf16_f32 v65, v66, v67
	ds_read2_b32 v[66:67], v77 offset0:140 offset1:173
	s_waitcnt lgkmcnt(0)
	v_cvt_pk_bf16_f32 v66, v66, v67
	ds_read2_b32 v[68:69], v77 offset0:206 offset1:239
	s_waitcnt lgkmcnt(0)
	v_cvt_pk_bf16_f32 v67, v68, v69
	v_add_u32_e32 v68, s0, v79
	v_ashrrev_i32_e32 v69, 31, v68
	v_lshlrev_b64 v[68:69], 12, v[68:69]
	v_lshl_add_u64 v[68:69], v[62:63], 0, v[68:69]
	global_store_dwordx4 v[68:69], v[64:67], off
	ds_read2_b32 v[64:65], v77 offset0:16 offset1:49
	s_waitcnt lgkmcnt(0)
	v_cvt_pk_bf16_f32 v64, v64, v65
	ds_read2_b32 v[66:67], v77 offset0:82 offset1:115
	s_waitcnt lgkmcnt(0)
	v_cvt_pk_bf16_f32 v65, v66, v67
	ds_read2_b32 v[66:67], v77 offset0:148 offset1:181
	s_waitcnt lgkmcnt(0)
	v_cvt_pk_bf16_f32 v66, v66, v67
	ds_read2_b32 v[68:69], v77 offset0:214 offset1:247
	s_waitcnt lgkmcnt(0)
	v_cvt_pk_bf16_f32 v67, v68, v69
	v_add_u32_e32 v68, s0, v80
	v_ashrrev_i32_e32 v69, 31, v68
	v_lshlrev_b64 v[68:69], 12, v[68:69]
	v_lshl_add_u64 v[68:69], v[62:63], 0, v[68:69]
	global_store_dwordx4 v[68:69], v[64:67], off
	ds_read2_b32 v[64:65], v77 offset0:24 offset1:57
	s_waitcnt lgkmcnt(0)
	v_cvt_pk_bf16_f32 v64, v64, v65
	ds_read2_b32 v[66:67], v77 offset0:90 offset1:123
	s_waitcnt lgkmcnt(0)
	v_cvt_pk_bf16_f32 v65, v66, v67
	ds_read2_b32 v[66:67], v77 offset0:156 offset1:189
	s_waitcnt lgkmcnt(0)
	v_cvt_pk_bf16_f32 v66, v66, v67
	ds_read2_b32 v[68:69], v77 offset0:222 offset1:255
	s_waitcnt lgkmcnt(0)
	v_cvt_pk_bf16_f32 v67, v68, v69
	v_add_u32_e32 v68, s0, v81
	v_ashrrev_i32_e32 v69, 31, v68
	v_lshlrev_b64 v[68:69], 12, v[68:69]
	v_lshl_add_u64 v[62:63], v[62:63], 0, v[68:69]
	global_store_dwordx4 v[62:63], v[64:67], off
	s_waitcnt lgkmcnt(0)

; __device__ __forceinline__ unsigned cvt_pk_bf16(float lo, float hi) { unsigned r; asm volatile("v_cvt_pk_bf16_f32 %0, %1, %2" : "=v"(r) : "v"(lo), "v"(hi)); return r; }
; #define LAS __attribute__((address_space(3)))
;     ...
; #pragma unroll 8
;     for (int i = 0; i < 32; ++i) { const int kk = 2 * i + (lane >> 5); scr[kk * 33 + (lane & 31)] = W[(size_t)(k0 + kk) * ldw + n0 + (lane & 31)]; }
;     asm volatile("s_waitcnt lgkmcnt(0)" ::: "memory");
;     const int c = lane & 7;
; #pragma unroll
;     for (int j = 0; j < 4; ++j) { const int n = (lane >> 3) + 8 * j; const LAS float* s = scr + (8 * c) * 33 + n;
;         v4u o; o.x = cvt_pk_bf16(s[0 * 33], s[1 * 33]); o.y = cvt_pk_bf16(s[2 * 33], s[3 * 33]); o.z = cvt_pk_bf16(s[4 * 33], s[5 * 33]); o.w = cvt_pk_bf16(s[6 * 33], s[7 * 33]);
;         *(v4u*)(WT + (size_t)(row_off + n0 + n) * ldt + ((koff + k0 + 8 * c) ^ kx)) = o; }
;     asm volatile("s_waitcnt lgkmcnt(0)" ::: "memory");
.LBB0_1274:
	s_lshl_b32 s23, s21, 1
	s_lshl_b32 s30, s1, 1
	v_add_u32_e32 v84, s23, v64
	v_add_u32_e32 v86, s30, v55
	v_mad_i64_i32 v[84:85], s[36:37], v84, s80, v[62:63]
	v_mad_i64_i32 v[86:87], s[36:37], v86, s80, v[62:63]
	global_load_dword v100, v[84:85], off
	global_load_dword v101, v[86:87], off
	v_add_u32_e32 v89, s23, v26
	v_add_u32_e32 v88, s30, v1
	v_mad_u64_u32 v[116:117], s[36:37], v89, s26, v[28:29]
	v_mad_u64_u32 v[118:119], s[36:37], v88, s26, v[28:29]
	v_add_u32_e32 v89, s23, v48
	v_add_u32_e32 v88, s30, v3
	s_add_i32 s21, s21, 16
	s_add_i32 s1, s1, 16
	s_add_i32 s22, s22, -16
	s_cmp_lg_u32 s22, 0
	v_add_u32_e32 v84, s23, v66
	v_add_u32_e32 v86, s30, v57
	v_mad_i64_i32 v[84:85], s[36:37], v84, s80, v[62:63]
	v_mad_i64_i32 v[86:87], s[36:37], v86, s80, v[62:63]
	global_load_dword v102, v[84:85], off
	global_load_dword v103, v[86:87], off
	v_mad_u64_u32 v[120:121], s[36:37], v89, s26, v[28:29]
	v_mad_u64_u32 v[122:123], s[36:37], v88, s26, v[28:29]
	v_add_u32_e32 v89, s23, v50
	v_add_u32_e32 v88, s30, v27
	v_add_u32_e32 v84, s23, v68
	v_add_u32_e32 v86, s30, v59
	v_mad_i64_i32 v[84:85], s[36:37], v84, s80, v[62:63]
	v_mad_i64_i32 v[86:87], s[36:37], v86, s80, v[62:63]
	global_load_dword v104, v[84:85], off
	global_load_dword v105, v[86:87], off
	v_mad_u64_u32 v[124:125], s[36:37], v89, s26, v[28:29]
	v_mad_u64_u32 v[126:127], s[36:37], v88, s26, v[28:29]
	v_add_u32_e32 v89, s23, v52
	v_add_u32_e32 v88, s30, v29
	v_add_u32_e32 v84, s23, v70
	v_add_u32_e32 v86, s30, v61
	v_mad_i64_i32 v[84:85], s[36:37], v84, s80, v[62:63]
	v_mad_i64_i32 v[86:87], s[36:37], v86, s80, v[62:63]
	global_load_dword v106, v[84:85], off
	global_load_dword v107, v[86:87], off
	v_mad_u64_u32 v[128:129], s[36:37], v89, s26, v[28:29]
	v_mad_u64_u32 v[130:131], s[36:37], v88, s26, v[28:29]
	v_add_u32_e32 v89, s23, v54
	v_add_u32_e32 v88, s30, v31
	v_add_u32_e32 v84, s23, v72
	v_add_u32_e32 v86, s30, v65
	v_mad_i64_i32 v[84:85], s[36:37], v84, s80, v[62:63]
	v_mad_i64_i32 v[86:87], s[36:37], v86, s80, v[62:63]
	global_load_dword v108, v[84:85], off
	global_load_dword v109, v[86:87], off
	v_mad_u64_u32 v[132:133], s[36:37], v89, s26, v[28:29]
	v_mad_u64_u32 v[134:135], s[36:37], v88, s26, v[28:29]
	v_add_u32_e32 v89, s23, v56
	v_add_u32_e32 v88, s30, v49
	v_add_u32_e32 v84, s23, v74
	v_add_u32_e32 v86, s30, v67
	v_mad_i64_i32 v[84:85], s[36:37], v84, s80, v[62:63]
	v_mad_i64_i32 v[86:87], s[36:37], v86, s80, v[62:63]
	global_load_dword v110, v[84:85], off
	global_load_dword v111, v[86:87], off
	v_mad_u64_u32 v[136:137], s[36:37], v89, s26, v[28:29]
	v_mad_u64_u32 v[138:139], s[36:37], v88, s26, v[28:29]
	v_add_u32_e32 v89, s23, v58
	v_add_u32_e32 v88, s30, v51
	v_add_u32_e32 v84, s23, v76
	v_add_u32_e32 v86, s30, v69
	v_mad_i64_i32 v[84:85], s[36:37], v84, s80, v[62:63]
	v_mad_i64_i32 v[86:87], s[36:37], v86, s80, v[62:63]
	global_load_dword v112, v[84:85], off
	global_load_dword v113, v[86:87], off
	v_mad_u64_u32 v[140:141], s[36:37], v89, s26, v[28:29]
	v_mad_u64_u32 v[142:143], s[36:37], v88, s26, v[28:29]
	v_add_u32_e32 v89, s23, v60
	v_add_u32_e32 v88, s30, v53
	v_add_u32_e32 v84, s23, v78
	v_add_u32_e32 v86, s30, v71
	v_mad_i64_i32 v[84:85], s[36:37], v84, s80, v[62:63]
	v_mad_i64_i32 v[86:87], s[36:37], v86, s80, v[62:63]
	global_load_dword v114, v[84:85], off
	global_load_dword v115, v[86:87], off
	v_mad_u64_u32 v[144:145], s[36:37], v89, s26, v[28:29]
	v_mad_u64_u32 v[146:147], s[36:37], v88, s26, v[28:29]
	s_waitcnt vmcnt(14)
	ds_write_b32 v116, v100
	ds_write_b32 v118, v101
	s_waitcnt vmcnt(12)
	ds_write_b32 v120, v102
	ds_write_b32 v122, v103
	s_waitcnt vmcnt(10)
	ds_write_b32 v124, v104
	ds_write_b32 v126, v105
	s_waitcnt vmcnt(8)
	ds_write_b32 v128, v106
	ds_write_b32 v130, v107
	s_waitcnt vmcnt(6)
	ds_write_b32 v132, v108
	ds_write_b32 v134, v109
	s_waitcnt vmcnt(4)
	ds_write_b32 v136, v110
	ds_write_b32 v138, v111
	s_waitcnt vmcnt(2)
	ds_write_b32 v140, v112
	ds_write_b32 v142, v113
	s_waitcnt vmcnt(0)
	ds_write_b32 v144, v114
	ds_write_b32 v146, v115
	s_cbranch_scc1 .LBB0_1274
	s_waitcnt lgkmcnt(0)
	ds_read2_b32 v[64:65], v77 offset1:33
	s_waitcnt lgkmcnt(0)
	v_cvt_pk_bf16_f32 v64, v64, v65
	ds_read2_b32 v[66:67], v77 offset0:66 offset1:99
	s_waitcnt lgkmcnt(0)
	v_cvt_pk_bf16_f32 v65, v66, v67
	ds_read2_b32 v[66:67], v77 offset0:132 offset1:165
	s_addk_i32 s5, 0x1600
	v_mov_b32_e32 v55, 0x400
	s_waitcnt lgkmcnt(0)
	v_cvt_pk_bf16_f32 v66, v66, v67
	ds_read2_b32 v[68:69], v77 offset0:198 offset1:231
	v_bitop3_b32 v55, s0, v55, v75 bitop3:0x36
	s_waitcnt lgkmcnt(0)
	v_cvt_pk_bf16_f32 v67, v68, v69
	v_add_u32_e32 v68, s5, v30
	v_lshlrev_b32_e32 v62, 1, v55
	v_mov_b32_e32 v63, v0
	v_ashrrev_i32_e32 v69, 31, v68
	v_lshl_add_u64 v[62:63], s[82:83], 0, v[62:63]
	v_lshlrev_b64 v[68:69], 12, v[68:69]
	v_lshl_add_u64 v[68:69], v[62:63], 0, v[68:69]
	global_store_dwordx4 v[68:69], v[64:67], off
	ds_read2_b32 v[64:65], v77 offset0:8 offset1:41
	s_waitcnt lgkmcnt(0)
	v_cvt_pk_bf16_f32 v64, v64, v65
	ds_read2_b32 v[66:67], v77 offset0:74 offset1:107
	s_waitcnt lgkmcnt(0)
	v_cvt_pk_bf16_f32 v65, v66, v67
	ds_read2_b32 v[66:67], v77 offset0:140 offset1:173
	s_waitcnt lgkmcnt(0)
	v_cvt_pk_bf16_f32 v66, v66, v67
	ds_read2_b32 v[68:69], v77 offset0:206 offset1:239
	s_waitcnt lgkmcnt(0)
	v_cvt_pk_bf16_f32 v67, v68, v69
	v_add_u32_e32 v68, s5, v79
	v_ashrrev_i32_e32 v69, 31, v68
	v_lshlrev_b64 v[68:69], 12, v[68:69]
	v_lshl_add_u64 v[68:69], v[62:63], 0, v[68:69]
	global_store_dwordx4 v[68:69], v[64:67], off
	ds_read2_b32 v[64:65], v77 offset0:16 offset1:49
	s_waitcnt lgkmcnt(0)
	v_cvt_pk_bf16_f32 v64, v64, v65
	ds_read2_b32 v[66:67], v77 offset0:82 offset1:115
	s_waitcnt lgkmcnt(0)
	v_cvt_pk_bf16_f32 v65, v66, v67
	ds_read2_b32 v[66:67], v77 offset0:148 offset1:181
	s_waitcnt lgkmcnt(0)
	v_cvt_pk_bf16_f32 v66, v66, v67
	ds_read2_b32 v[68:69], v77 offset0:214 offset1:247
	s_waitcnt lgkmcnt(0)
	v_cvt_pk_bf16_f32 v67, v68, v69
	v_add_u32_e32 v68, s5, v80
	v_ashrrev_i32_e32 v69, 31, v68
	v_lshlrev_b64 v[68:69], 12, v[68:69]
	v_lshl_add_u64 v[68:69], v[62:63], 0, v[68:69]
	global_store_dwordx4 v[68:69], v[64:67], off
	ds_read2_b32 v[64:65], v77 offset0:24 offset1:57
	s_waitcnt lgkmcnt(0)
	v_cvt_pk_bf16_f32 v64, v64, v65
	ds_read2_b32 v[66:67], v77 offset0:90 offset1:123
	s_waitcnt lgkmcnt(0)
	v_cvt_pk_bf16_f32 v65, v66, v67
	ds_read2_b32 v[66:67], v77 offset0:156 offset1:189
	s_waitcnt lgkmcnt(0)
	v_cvt_pk_bf16_f32 v66, v66, v67
	ds_read2_b32 v[68:69], v77 offset0:222 offset1:255
	s_waitcnt lgkmcnt(0)
	v_cvt_pk_bf16_f32 v67, v68, v69
	v_add_u32_e32 v68, s5, v81
	v_ashrrev_i32_e32 v69, 31, v68
	v_lshlrev_b64 v[68:69], 12, v[68:69]
	v_lshl_add_u64 v[62:63], v[62:63], 0, v[68:69]
	global_store_dwordx4 v[62:63], v[64:67], off
	s_waitcnt lgkmcnt(0)

; __device__ __forceinline__ unsigned cvt_pk_bf16(float lo, float hi) { unsigned r; asm volatile("v_cvt_pk_bf16_f32 %0, %1, %2" : "=v"(r) : "v"(lo), "v"(hi)); return r; }
; #define LAS __attribute__((address_space(3)))
;     ...
; #pragma unroll 8
;     for (int i = 0; i < 32; ++i) { const int kk = 2 * i + (lane >> 5); scr[kk * 33 + (lane & 31)] = W[(size_t)(k0 + kk) * ldw + n0 + (lane & 31)]; }
;     asm volatile("s_waitcnt lgkmcnt(0)" ::: "memory");
;     const int c = lane & 7;
; #pragma unroll
;     for (int j = 0; j < 4; ++j) { const int n = (lane >> 3) + 8 * j; const LAS float* s = scr + (8 * c) * 33 + n;
;         v4u o; o.x = cvt_pk_bf16(s[0 * 33], s[1 * 33]); o.y = cvt_pk_bf16(s[2 * 33], s[3 * 33]); o.z = cvt_pk_bf16(s[4 * 33], s[5 * 33]); o.w = cvt_pk_bf16(s[6 * 33], s[7 * 33]);
;         *(v4u*)(WT + (size_t)(row_off + n0 + n) * ldt + ((koff + k0 + 8 * c) ^ kx)) = o; }
;     asm volatile("s_waitcnt lgkmcnt(0)" ::: "memory");
.LBB0_1279:
	s_lshl_b32 s23, s21, 1
	s_lshl_b32 s30, s5, 1
	v_add_u32_e32 v84, s23, v64
	v_add_u32_e32 v86, s30, v55
	v_mad_i64_i32 v[84:85], s[36:37], v84, s80, v[62:63]
	v_mad_i64_i32 v[86:87], s[36:37], v86, s80, v[62:63]
	global_load_dword v100, v[84:85], off
	global_load_dword v101, v[86:87], off
	v_add_u32_e32 v89, s23, v26
	v_add_u32_e32 v88, s30, v1
	v_mad_u64_u32 v[116:117], s[36:37], v89, s26, v[28:29]
	v_mad_u64_u32 v[118:119], s[36:37], v88, s26, v[28:29]
	v_add_u32_e32 v89, s23, v48
	v_add_u32_e32 v88, s30, v3
	s_add_i32 s21, s21, 16
	s_add_i32 s5, s5, 16
	s_add_i32 s22, s22, -16
	s_cmp_lg_u32 s22, 0
	v_add_u32_e32 v84, s23, v66
	v_add_u32_e32 v86, s30, v57
	v_mad_i64_i32 v[84:85], s[36:37], v84, s80, v[62:63]
	v_mad_i64_i32 v[86:87], s[36:37], v86, s80, v[62:63]
	global_load_dword v102, v[84:85], off
	global_load_dword v103, v[86:87], off
	v_mad_u64_u32 v[120:121], s[36:37], v89, s26, v[28:29]
	v_mad_u64_u32 v[122:123], s[36:37], v88, s26, v[28:29]
	v_add_u32_e32 v89, s23, v50
	v_add_u32_e32 v88, s30, v27
	v_add_u32_e32 v84, s23, v68
	v_add_u32_e32 v86, s30, v59
	v_mad_i64_i32 v[84:85], s[36:37], v84, s80, v[62:63]
	v_mad_i64_i32 v[86:87], s[36:37], v86, s80, v[62:63]
	global_load_dword v104, v[84:85], off
	global_load_dword v105, v[86:87], off
	v_mad_u64_u32 v[124:125], s[36:37], v89, s26, v[28:29]
	v_mad_u64_u32 v[126:127], s[36:37], v88, s26, v[28:29]
	v_add_u32_e32 v89, s23, v52
	v_add_u32_e32 v88, s30, v29
	v_add_u32_e32 v84, s23, v70
	v_add_u32_e32 v86, s30, v61
	v_mad_i64_i32 v[84:85], s[36:37], v84, s80, v[62:63]
	v_mad_i64_i32 v[86:87], s[36:37], v86, s80, v[62:63]
	global_load_dword v106, v[84:85], off
	global_load_dword v107, v[86:87], off
	v_mad_u64_u32 v[128:129], s[36:37], v89, s26, v[28:29]
	v_mad_u64_u32 v[130:131], s[36:37], v88, s26, v[28:29]
	v_add_u32_e32 v89, s23, v54
	v_add_u32_e32 v88, s30, v31
	v_add_u32_e32 v84, s23, v72
	v_add_u32_e32 v86, s30, v65
	v_mad_i64_i32 v[84:85], s[36:37], v84, s80, v[62:63]
	v_mad_i64_i32 v[86:87], s[36:37], v86, s80, v[62:63]
	global_load_dword v108, v[84:85], off
	global_load_dword v109, v[86:87], off
	v_mad_u64_u32 v[132:133], s[36:37], v89, s26, v[28:29]
	v_mad_u64_u32 v[134:135], s[36:37], v88, s26, v[28:29]
	v_add_u32_e32 v89, s23, v56
	v_add_u32_e32 v88, s30, v49
	v_add_u32_e32 v84, s23, v74
	v_add_u32_e32 v86, s30, v67
	v_mad_i64_i32 v[84:85], s[36:37], v84, s80, v[62:63]
	v_mad_i64_i32 v[86:87], s[36:37], v86, s80, v[62:63]
	global_load_dword v110, v[84:85], off
	global_load_dword v111, v[86:87], off
	v_mad_u64_u32 v[136:137], s[36:37], v89, s26, v[28:29]
	v_mad_u64_u32 v[138:139], s[36:37], v88, s26, v[28:29]
	v_add_u32_e32 v89, s23, v58
	v_add_u32_e32 v88, s30, v51
	v_add_u32_e32 v84, s23, v76
	v_add_u32_e32 v86, s30, v69
	v_mad_i64_i32 v[84:85], s[36:37], v84, s80, v[62:63]
	v_mad_i64_i32 v[86:87], s[36:37], v86, s80, v[62:63]
	global_load_dword v112, v[84:85], off
	global_load_dword v113, v[86:87], off
	v_mad_u64_u32 v[140:141], s[36:37], v89, s26, v[28:29]
	v_mad_u64_u32 v[142:143], s[36:37], v88, s26, v[28:29]
	v_add_u32_e32 v89, s23, v60
	v_add_u32_e32 v88, s30, v53
	v_add_u32_e32 v84, s23, v78
	v_add_u32_e32 v86, s30, v71
	v_mad_i64_i32 v[84:85], s[36:37], v84, s80, v[62:63]
	v_mad_i64_i32 v[86:87], s[36:37], v86, s80, v[62:63]
	global_load_dword v114, v[84:85], off
	global_load_dword v115, v[86:87], off
	v_mad_u64_u32 v[144:145], s[36:37], v89, s26, v[28:29]
	v_mad_u64_u32 v[146:147], s[36:37], v88, s26, v[28:29]
	s_waitcnt vmcnt(14)
	ds_write_b32 v116, v100
	ds_write_b32 v118, v101
	s_waitcnt vmcnt(12)
	ds_write_b32 v120, v102
	ds_write_b32 v122, v103
	s_waitcnt vmcnt(10)
	ds_write_b32 v124, v104
	ds_write_b32 v126, v105
	s_waitcnt vmcnt(8)
	ds_write_b32 v128, v106
	ds_write_b32 v130, v107
	s_waitcnt vmcnt(6)
	ds_write_b32 v132, v108
	ds_write_b32 v134, v109
	s_waitcnt vmcnt(4)
	ds_write_b32 v136, v110
	ds_write_b32 v138, v111
	s_waitcnt vmcnt(2)
	ds_write_b32 v140, v112
	ds_write_b32 v142, v113
	s_waitcnt vmcnt(0)
	ds_write_b32 v144, v114
	ds_write_b32 v146, v115
	s_cbranch_scc1 .LBB0_1279
	s_waitcnt lgkmcnt(0)
	ds_read2_b32 v[64:65], v77 offset1:33
	s_waitcnt lgkmcnt(0)
	v_cvt_pk_bf16_f32 v64, v64, v65
	ds_read2_b32 v[66:67], v77 offset0:66 offset1:99
	s_waitcnt lgkmcnt(0)
	v_cvt_pk_bf16_f32 v65, v66, v67
	ds_read2_b32 v[66:67], v77 offset0:132 offset1:165
	s_addk_i32 s1, 0xe00
	v_mov_b32_e32 v55, 0x400
	s_waitcnt lgkmcnt(0)
	v_cvt_pk_bf16_f32 v66, v66, v67
	ds_read2_b32 v[68:69], v77 offset0:198 offset1:231
	v_bitop3_b32 v55, s0, v55, v75 bitop3:0x36
	s_waitcnt lgkmcnt(0)
	v_cvt_pk_bf16_f32 v67, v68, v69
	v_add_u32_e32 v68, s1, v30
	v_lshlrev_b32_e32 v62, 1, v55
	v_mov_b32_e32 v63, v0
	v_ashrrev_i32_e32 v69, 31, v68
	v_lshl_add_u64 v[62:63], s[82:83], 0, v[62:63]
	v_lshlrev_b64 v[68:69], 12, v[68:69]
	v_lshl_add_u64 v[68:69], v[62:63], 0, v[68:69]
	global_store_dwordx4 v[68:69], v[64:67], off
	ds_read2_b32 v[64:65], v77 offset0:8 offset1:41
	s_waitcnt lgkmcnt(0)
	v_cvt_pk_bf16_f32 v64, v64, v65
	ds_read2_b32 v[66:67], v77 offset0:74 offset1:107
	s_waitcnt lgkmcnt(0)
	v_cvt_pk_bf16_f32 v65, v66, v67
	ds_read2_b32 v[66:67], v77 offset0:140 offset1:173
	s_waitcnt lgkmcnt(0)
	v_cvt_pk_bf16_f32 v66, v66, v67
	ds_read2_b32 v[68:69], v77 offset0:206 offset1:239
	s_waitcnt lgkmcnt(0)
	v_cvt_pk_bf16_f32 v67, v68, v69
	v_add_u32_e32 v68, s1, v79
	v_ashrrev_i32_e32 v69, 31, v68
	v_lshlrev_b64 v[68:69], 12, v[68:69]
	v_lshl_add_u64 v[68:69], v[62:63], 0, v[68:69]
	global_store_dwordx4 v[68:69], v[64:67], off
	ds_read2_b32 v[64:65], v77 offset0:16 offset1:49
	s_waitcnt lgkmcnt(0)
	v_cvt_pk_bf16_f32 v64, v64, v65
	ds_read2_b32 v[66:67], v77 offset0:82 offset1:115
	s_waitcnt lgkmcnt(0)
	v_cvt_pk_bf16_f32 v65, v66, v67
	ds_read2_b32 v[66:67], v77 offset0:148 offset1:181
	s_waitcnt lgkmcnt(0)
	v_cvt_pk_bf16_f32 v66, v66, v67
	ds_read2_b32 v[68:69], v77 offset0:214 offset1:247
	s_waitcnt lgkmcnt(0)
	v_cvt_pk_bf16_f32 v67, v68, v69
	v_add_u32_e32 v68, s1, v80
	v_ashrrev_i32_e32 v69, 31, v68
	v_lshlrev_b64 v[68:69], 12, v[68:69]
	v_lshl_add_u64 v[68:69], v[62:63], 0, v[68:69]
	global_store_dwordx4 v[68:69], v[64:67], off
	ds_read2_b32 v[64:65], v77 offset0:24 offset1:57
	s_waitcnt lgkmcnt(0)
	v_cvt_pk_bf16_f32 v64, v64, v65
	ds_read2_b32 v[66:67], v77 offset0:90 offset1:123
	s_waitcnt lgkmcnt(0)
	v_cvt_pk_bf16_f32 v65, v66, v67
	ds_read2_b32 v[66:67], v77 offset0:156 offset1:189
	s_waitcnt lgkmcnt(0)
	v_cvt_pk_bf16_f32 v66, v66, v67
	ds_read2_b32 v[68:69], v77 offset0:222 offset1:255
	s_waitcnt lgkmcnt(0)
	v_cvt_pk_bf16_f32 v67, v68, v69
	v_add_u32_e32 v68, s1, v81
	v_ashrrev_i32_e32 v69, 31, v68
	v_lshlrev_b64 v[68:69], 12, v[68:69]
	v_lshl_add_u64 v[62:63], v[62:63], 0, v[68:69]
	global_store_dwordx4 v[62:63], v[64:67], off
	s_waitcnt lgkmcnt(0)

; __device__ __forceinline__ unsigned cvt_pk_bf16(float lo, float hi) { unsigned r; asm volatile("v_cvt_pk_bf16_f32 %0, %1, %2" : "=v"(r) : "v"(lo), "v"(hi)); return r; }
; #define LAS __attribute__((address_space(3)))
;     ...
; #pragma unroll 8
;     for (int i = 0; i < 32; ++i) { const int kk = 2 * i + (lane >> 5); scr[kk * 33 + (lane & 31)] = W[(size_t)(k0 + kk) * ldw + n0 + (lane & 31)]; }
;     asm volatile("s_waitcnt lgkmcnt(0)" ::: "memory");
;     const int c = lane & 7;
; #pragma unroll
;     for (int j = 0; j < 4; ++j) { const int n = (lane >> 3) + 8 * j; const LAS float* s = scr + (8 * c) * 33 + n;
;         v4u o; o.x = cvt_pk_bf16(s[0 * 33], s[1 * 33]); o.y = cvt_pk_bf16(s[2 * 33], s[3 * 33]); o.z = cvt_pk_bf16(s[4 * 33], s[5 * 33]); o.w = cvt_pk_bf16(s[6 * 33], s[7 * 33]);
;         *(v4u*)(WT + (size_t)(row_off + n0 + n) * ldt + ((koff + k0 + 8 * c) ^ kx)) = o; }
;     asm volatile("s_waitcnt lgkmcnt(0)" ::: "memory");
.LBB0_1284:
	s_lshl_b32 s23, s21, 1
	s_lshl_b32 s30, s1, 1
	v_add_u32_e32 v84, s23, v64
	v_add_u32_e32 v86, s30, v55
	v_mad_i64_i32 v[84:85], s[36:37], v84, s80, v[62:63]
	v_mad_i64_i32 v[86:87], s[36:37], v86, s80, v[62:63]
	global_load_dword v100, v[84:85], off
	global_load_dword v101, v[86:87], off
	v_add_u32_e32 v89, s23, v26
	v_add_u32_e32 v88, s30, v1
	v_mad_u64_u32 v[116:117], s[36:37], v89, s26, v[28:29]
	v_mad_u64_u32 v[118:119], s[36:37], v88, s26, v[28:29]
	v_add_u32_e32 v89, s23, v48
	v_add_u32_e32 v88, s30, v3
	s_add_i32 s21, s21, 16
	s_add_i32 s1, s1, 16
	s_add_i32 s22, s22, -16
	s_cmp_lg_u32 s22, 0
	v_add_u32_e32 v84, s23, v66
	v_add_u32_e32 v86, s30, v57
	v_mad_i64_i32 v[84:85], s[36:37], v84, s80, v[62:63]
	v_mad_i64_i32 v[86:87], s[36:37], v86, s80, v[62:63]
	global_load_dword v102, v[84:85], off
	global_load_dword v103, v[86:87], off
	v_mad_u64_u32 v[120:121], s[36:37], v89, s26, v[28:29]
	v_mad_u64_u32 v[122:123], s[36:37], v88, s26, v[28:29]
	v_add_u32_e32 v89, s23, v50
	v_add_u32_e32 v88, s30, v27
	v_add_u32_e32 v84, s23, v68
	v_add_u32_e32 v86, s30, v59
	v_mad_i64_i32 v[84:85], s[36:37], v84, s80, v[62:63]
	v_mad_i64_i32 v[86:87], s[36:37], v86, s80, v[62:63]
	global_load_dword v104, v[84:85], off
	global_load_dword v105, v[86:87], off
	v_mad_u64_u32 v[124:125], s[36:37], v89, s26, v[28:29]
	v_mad_u64_u32 v[126:127], s[36:37], v88, s26, v[28:29]
	v_add_u32_e32 v89, s23, v52
	v_add_u32_e32 v88, s30, v29
	v_add_u32_e32 v84, s23, v70
	v_add_u32_e32 v86, s30, v61
	v_mad_i64_i32 v[84:85], s[36:37], v84, s80, v[62:63]
	v_mad_i64_i32 v[86:87], s[36:37], v86, s80, v[62:63]
	global_load_dword v106, v[84:85], off
	global_load_dword v107, v[86:87], off
	v_mad_u64_u32 v[128:129], s[36:37], v89, s26, v[28:29]
	v_mad_u64_u32 v[130:131], s[36:37], v88, s26, v[28:29]
	v_add_u32_e32 v89, s23, v54
	v_add_u32_e32 v88, s30, v31
	v_add_u32_e32 v84, s23, v72
	v_add_u32_e32 v86, s30, v65
	v_mad_i64_i32 v[84:85], s[36:37], v84, s80, v[62:63]
	v_mad_i64_i32 v[86:87], s[36:37], v86, s80, v[62:63]
	global_load_dword v108, v[84:85], off
	global_load_dword v109, v[86:87], off
	v_mad_u64_u32 v[132:133], s[36:37], v89, s26, v[28:29]
	v_mad_u64_u32 v[134:135], s[36:37], v88, s26, v[28:29]
	v_add_u32_e32 v89, s23, v56
	v_add_u32_e32 v88, s30, v49
	v_add_u32_e32 v84, s23, v74
	v_add_u32_e32 v86, s30, v67
	v_mad_i64_i32 v[84:85], s[36:37], v84, s80, v[62:63]
	v_mad_i64_i32 v[86:87], s[36:37], v86, s80, v[62:63]
	global_load_dword v110, v[84:85], off
	global_load_dword v111, v[86:87], off
	v_mad_u64_u32 v[136:137], s[36:37], v89, s26, v[28:29]
	v_mad_u64_u32 v[138:139], s[36:37], v88, s26, v[28:29]
	v_add_u32_e32 v89, s23, v58
	v_add_u32_e32 v88, s30, v51
	v_add_u32_e32 v84, s23, v76
	v_add_u32_e32 v86, s30, v69
	v_mad_i64_i32 v[84:85], s[36:37], v84, s80, v[62:63]
	v_mad_i64_i32 v[86:87], s[36:37], v86, s80, v[62:63]
	global_load_dword v112, v[84:85], off
	global_load_dword v113, v[86:87], off
	v_mad_u64_u32 v[140:141], s[36:37], v89, s26, v[28:29]
	v_mad_u64_u32 v[142:143], s[36:37], v88, s26, v[28:29]
	v_add_u32_e32 v89, s23, v60
	v_add_u32_e32 v88, s30, v53
	v_add_u32_e32 v84, s23, v78
	v_add_u32_e32 v86, s30, v71
	v_mad_i64_i32 v[84:85], s[36:37], v84, s80, v[62:63]
	v_mad_i64_i32 v[86:87], s[36:37], v86, s80, v[62:63]
	global_load_dword v114, v[84:85], off
	global_load_dword v115, v[86:87], off
	v_mad_u64_u32 v[144:145], s[36:37], v89, s26, v[28:29]
	v_mad_u64_u32 v[146:147], s[36:37], v88, s26, v[28:29]
	s_waitcnt vmcnt(14)
	ds_write_b32 v116, v100
	ds_write_b32 v118, v101
	s_waitcnt vmcnt(12)
	ds_write_b32 v120, v102
	ds_write_b32 v122, v103
	s_waitcnt vmcnt(10)
	ds_write_b32 v124, v104
	ds_write_b32 v126, v105
	s_waitcnt vmcnt(8)
	ds_write_b32 v128, v106
	ds_write_b32 v130, v107
	s_waitcnt vmcnt(6)
	ds_write_b32 v132, v108
	ds_write_b32 v134, v109
	s_waitcnt vmcnt(4)
	ds_write_b32 v136, v110
	ds_write_b32 v138, v111
	s_waitcnt vmcnt(2)
	ds_write_b32 v140, v112
	ds_write_b32 v142, v113
	s_waitcnt vmcnt(0)
	ds_write_b32 v144, v114
	ds_write_b32 v146, v115
	s_cbranch_scc1 .LBB0_1284
	s_waitcnt lgkmcnt(0)
	ds_read2_b32 v[64:65], v77 offset1:33
	s_waitcnt lgkmcnt(0)
	v_cvt_pk_bf16_f32 v64, v64, v65
	ds_read2_b32 v[66:67], v77 offset0:66 offset1:99
	s_waitcnt lgkmcnt(0)
	v_cvt_pk_bf16_f32 v65, v66, v67
	ds_read2_b32 v[66:67], v77 offset0:132 offset1:165
	v_mov_b32_e32 v55, 0x400
	s_waitcnt lgkmcnt(0)
	v_cvt_pk_bf16_f32 v66, v66, v67
	ds_read2_b32 v[68:69], v77 offset0:198 offset1:231
	v_bitop3_b32 v62, s5, v55, v75 bitop3:0x36
	s_waitcnt lgkmcnt(0)
	v_cvt_pk_bf16_f32 v67, v68, v69
	v_add_u32_e32 v68, s0, v30
	v_ashrrev_i32_e32 v63, 31, v62
	v_ashrrev_i32_e32 v69, 31, v68
	v_lshl_add_u64 v[62:63], v[62:63], 1, s[82:83]
	v_lshlrev_b64 v[68:69], 12, v[68:69]
	v_lshl_add_u64 v[68:69], v[62:63], 0, v[68:69]
	global_store_dwordx4 v[68:69], v[64:67], off
	ds_read2_b32 v[64:65], v77 offset0:8 offset1:41
	s_waitcnt lgkmcnt(0)
	v_cvt_pk_bf16_f32 v64, v64, v65
	ds_read2_b32 v[66:67], v77 offset0:74 offset1:107
	s_waitcnt lgkmcnt(0)
	v_cvt_pk_bf16_f32 v65, v66, v67
	ds_read2_b32 v[66:67], v77 offset0:140 offset1:173
	s_waitcnt lgkmcnt(0)
	v_cvt_pk_bf16_f32 v66, v66, v67
	ds_read2_b32 v[68:69], v77 offset0:206 offset1:239
	s_waitcnt lgkmcnt(0)
	v_cvt_pk_bf16_f32 v67, v68, v69
	v_add_u32_e32 v68, s0, v79
	v_ashrrev_i32_e32 v69, 31, v68
	v_lshlrev_b64 v[68:69], 12, v[68:69]
	v_lshl_add_u64 v[68:69], v[62:63], 0, v[68:69]
	global_store_dwordx4 v[68:69], v[64:67], off
	ds_read2_b32 v[64:65], v77 offset0:16 offset1:49
	s_waitcnt lgkmcnt(0)
	v_cvt_pk_bf16_f32 v64, v64, v65
	ds_read2_b32 v[66:67], v77 offset0:82 offset1:115
	s_waitcnt lgkmcnt(0)
	v_cvt_pk_bf16_f32 v65, v66, v67
	ds_read2_b32 v[66:67], v77 offset0:148 offset1:181
	s_waitcnt lgkmcnt(0)
	v_cvt_pk_bf16_f32 v66, v66, v67
	ds_read2_b32 v[68:69], v77 offset0:214 offset1:247
	s_waitcnt lgkmcnt(0)
	v_cvt_pk_bf16_f32 v67, v68, v69
	v_add_u32_e32 v68, s0, v80
	v_ashrrev_i32_e32 v69, 31, v68
	v_lshlrev_b64 v[68:69], 12, v[68:69]
	v_lshl_add_u64 v[68:69], v[62:63], 0, v[68:69]
	global_store_dwordx4 v[68:69], v[64:67], off
	ds_read2_b32 v[64:65], v77 offset0:24 offset1:57
	s_waitcnt lgkmcnt(0)
	v_cvt_pk_bf16_f32 v64, v64, v65
	ds_read2_b32 v[66:67], v77 offset0:90 offset1:123
	s_waitcnt lgkmcnt(0)
	v_cvt_pk_bf16_f32 v65, v66, v67
	ds_read2_b32 v[66:67], v77 offset0:156 offset1:189
	s_waitcnt lgkmcnt(0)
	v_cvt_pk_bf16_f32 v66, v66, v67
	ds_read2_b32 v[68:69], v77 offset0:222 offset1:255
	s_waitcnt lgkmcnt(0)
	v_cvt_pk_bf16_f32 v67, v68, v69
	v_add_u32_e32 v68, s0, v81
	v_ashrrev_i32_e32 v69, 31, v68
	v_lshlrev_b64 v[68:69], 12, v[68:69]
	v_lshl_add_u64 v[62:63], v[62:63], 0, v[68:69]
	global_store_dwordx4 v[62:63], v[64:67], off
	s_waitcnt lgkmcnt(0)
	s_branch .LBB0_1201
